# attention rewrite: bias/mask registers and sink term computed once per wave (head is constant), q register sets alternate (no copies)
# baseline (speedup 1.0000x reference)
.LBB0_1396:
	s_or_b64 exec, exec, s[6:7]
	s_add_u32 s14, s12, 0x18000000
	s_addc_u32 s15, s13, 0
	s_add_u32 s16, s12, 0x2a000000
	s_addc_u32 s17, s13, 0
	s_add_u32 s30, s12, 0x22000000
	s_addc_u32 s31, s13, 0
	v_readfirstlane_b32 s33, v0
	v_and_b32_e32 v2, 15, v242
	v_lshrrev_b32_e32 v3, 4, v242
	s_lshr_b32 s33, s33, 6
	v_lshrrev_b32_e32 v232, 1, v0
	v_and_b32_e32 v233, 1, v0
	v_mul_u32_u24_e32 v4, 0x90, v232
	v_lshl_add_u32 v4, v233, 6, v4
	v_mul_u32_u24_e32 v6, 0x1400, v232
	v_lshl_add_u32 v6, v233, 6, v6
	v_lshlrev_b32_e32 v234, 7, v233
	v_add_u32_e32 v19, 0x15400, v234
	v_lshrrev_b32_e32 v232, 3, v0
	v_and_b32_e32 v233, 7, v0
	v_mul_u32_u24_e32 v5, 0x210, v232
	v_lshl_add_u32 v5, v233, 4, v5
	v_add_u32_e32 v5, 0x9000, v5
	v_lshlrev_b32_e32 v7, 15, v232
	v_lshl_add_u32 v7, v233, 4, v7
	v_mul_u32_u24_e32 v8, 0x1400, v2
	v_lshl_add_u32 v8, v3, 4, v8
	v_lshlrev_b32_e32 v9, 12, v2
	v_lshl_add_u32 v9, v3, 3, v9
	v_mul_u32_u24_e32 v10, 0x90, v2
	v_lshl_add_u32 v10, v3, 4, v10
	v_mul_u32_u24_e32 v11, 0x210, v2
	v_lshl_add_u32 v11, v3, 3, v11
	v_add_u32_e32 v11, 0x9000, v11
	v_add_u32_e32 v12, 0x2100, v11
	v_add_u32_e32 v13, 0x4200, v11
	v_add_u32_e32 v14, 0x6300, v11
	v_xor_b32_e32 v15, 16, v242
	v_lshlrev_b32_e32 v15, 2, v15
	v_xor_b32_e32 v16, 32, v242
	v_lshlrev_b32_e32 v16, 2, v16
	v_xor_b32_e32 v17, 1, v242
	v_lshlrev_b32_e32 v17, 2, v17
	v_lshlrev_b32_e32 v232, 2, v3
	v_sub_u32_e32 v18, v2, v232
	v_add_u32_e32 v18, 0x80, v18
	v_mov_b32_e32 v89, 0xff800000
	v_mov_b32_e32 v90, 0
	s_mov_b32 s34, s96
	s_mov_b32 s55, -1
	s_waitcnt lgkmcnt(0)
	s_barrier
	s_cmpk_gt_u32 s34, 0x3ff
	s_cbranch_scc1 .Lat_done
	s_and_b32 s3, s34, 3
	s_bfe_u32 s4, s34, 0x70002
	s_lshr_b32 s5, s34, 9
	s_lshl_b32 s6, s5, 14
	s_lshl_b32 s7, s4, 7
	s_add_i32 s6, s6, s7
	s_sub_i32 s6, s6, 0x80
	s_mul_i32 s7, s6, 0x1400
	s_ashr_i32 s9, s7, 31
	s_add_u32 s40, s14, s7
	s_addc_u32 s41, s15, s9
	s_lshl_b32 s7, s3, 7
	s_add_u32 s40, s40, s7
	s_addc_u32 s41, s41, 0
	s_lshl_b32 s6, s5, 2
	s_add_i32 s6, s6, s3
	s_lshl_b32 s6, s6, 21
	s_lshl_b32 s7, s4, 8
	s_sub_i32 s7, s7, 0x100
	s_add_i32 s6, s6, s7
	s_ashr_i32 s7, s6, 31
	s_add_u32 s42, s16, s6
	s_addc_u32 s43, s17, s7
	global_load_dwordx4 v[20:23], v6, s[40:41] offset:0
	global_load_dwordx4 v[24:27], v6, s[40:41] offset:16
	global_load_dwordx4 v[28:31], v6, s[40:41] offset:32
	global_load_dwordx4 v[32:35], v6, s[40:41] offset:48
	global_load_dwordx4 v[36:39], v7, s[42:43] offset:0
	global_load_dwordx4 v[40:43], v7, s[42:43] offset:128
	global_load_dwordx4 v[44:47], v7, s[42:43] offset:256
	global_load_dwordx4 v[48:51], v7, s[42:43] offset:384

.Lat_pfd:
	s_cmp_eq_u32 s38, s55
	s_cbranch_scc1 .Lat_bzdone
	s_mov_b32 s55, s38
	v_mov_b32_e32 v232, s54
	v_mul_f32_e32 v232, 0x3fb8aa3b, v232
	v_add_f32_e32 v232, 0xc1800000, v232
	v_exp_f32_e32 v88, v232
	s_lshl_b32 s2, s38, 9
	s_add_i32 s2, s2, 0x11400
	v_subrev_u32_e32 v233, 0, v18
	v_and_b32_e32 v233, 0x7f, v233
	v_lshl_add_u32 v233, v233, 2, s2
	ds_read_b32 v52, v233
	v_subrev_u32_e32 v233, 1, v18
	v_and_b32_e32 v233, 0x7f, v233
	v_lshl_add_u32 v233, v233, 2, s2
	ds_read_b32 v53, v233
	v_subrev_u32_e32 v233, 2, v18
	v_and_b32_e32 v233, 0x7f, v233
	v_lshl_add_u32 v233, v233, 2, s2
	ds_read_b32 v54, v233
	v_subrev_u32_e32 v233, 3, v18
	v_and_b32_e32 v233, 0x7f, v233
	v_lshl_add_u32 v233, v233, 2, s2
	ds_read_b32 v55, v233
	v_subrev_u32_e32 v233, 16, v18
	v_and_b32_e32 v233, 0x7f, v233
	v_lshl_add_u32 v233, v233, 2, s2
	ds_read_b32 v56, v233
	v_subrev_u32_e32 v233, 17, v18
	v_and_b32_e32 v233, 0x7f, v233
	v_lshl_add_u32 v233, v233, 2, s2
	ds_read_b32 v57, v233
	v_subrev_u32_e32 v233, 18, v18
	v_and_b32_e32 v233, 0x7f, v233
	v_lshl_add_u32 v233, v233, 2, s2
	ds_read_b32 v58, v233
	v_subrev_u32_e32 v233, 19, v18
	v_and_b32_e32 v233, 0x7f, v233
	v_lshl_add_u32 v233, v233, 2, s2
	ds_read_b32 v59, v233
	v_subrev_u32_e32 v233, 32, v18
	v_and_b32_e32 v233, 0x7f, v233
	v_lshl_add_u32 v233, v233, 2, s2
	ds_read_b32 v60, v233
	v_subrev_u32_e32 v233, 33, v18
	v_and_b32_e32 v233, 0x7f, v233
	v_lshl_add_u32 v233, v233, 2, s2
	ds_read_b32 v61, v233
	v_subrev_u32_e32 v233, 34, v18
	v_and_b32_e32 v233, 0x7f, v233
	v_lshl_add_u32 v233, v233, 2, s2
	ds_read_b32 v62, v233
	v_subrev_u32_e32 v233, 35, v18
	v_and_b32_e32 v233, 0x7f, v233
	v_lshl_add_u32 v233, v233, 2, s2
	ds_read_b32 v63, v233
	s_waitcnt lgkmcnt(0)
	v_subrev_u32_e32 v233, 48, v18
	v_and_b32_e32 v233, 0x7f, v233
	v_lshl_add_u32 v233, v233, 2, s2
	ds_read_b32 v64, v233
	v_subrev_u32_e32 v233, 49, v18
	v_and_b32_e32 v233, 0x7f, v233
	v_lshl_add_u32 v233, v233, 2, s2
	ds_read_b32 v65, v233
	v_subrev_u32_e32 v233, 50, v18
	v_and_b32_e32 v233, 0x7f, v233
	v_lshl_add_u32 v233, v233, 2, s2
	ds_read_b32 v66, v233
	v_subrev_u32_e32 v233, 51, v18
	v_and_b32_e32 v233, 0x7f, v233
	v_lshl_add_u32 v233, v233, 2, s2
	ds_read_b32 v67, v233
	v_subrev_u32_e32 v233, 64, v18
	v_and_b32_e32 v233, 0x7f, v233
	v_lshl_add_u32 v233, v233, 2, s2
	ds_read_b32 v68, v233
	v_subrev_u32_e32 v233, 0x41, v18
	v_and_b32_e32 v233, 0x7f, v233
	v_lshl_add_u32 v233, v233, 2, s2
	ds_read_b32 v69, v233
	v_subrev_u32_e32 v233, 0x42, v18
	v_and_b32_e32 v233, 0x7f, v233
	v_lshl_add_u32 v233, v233, 2, s2
	ds_read_b32 v70, v233
	v_subrev_u32_e32 v233, 0x43, v18
	v_and_b32_e32 v233, 0x7f, v233
	v_lshl_add_u32 v233, v233, 2, s2
	ds_read_b32 v71, v233
	v_subrev_u32_e32 v233, 0x50, v18
	v_and_b32_e32 v233, 0x7f, v233
	v_lshl_add_u32 v233, v233, 2, s2
	ds_read_b32 v72, v233
	v_subrev_u32_e32 v233, 0x51, v18
	v_and_b32_e32 v233, 0x7f, v233
	v_lshl_add_u32 v233, v233, 2, s2
	ds_read_b32 v73, v233
	v_subrev_u32_e32 v233, 0x52, v18
	v_and_b32_e32 v233, 0x7f, v233
	v_lshl_add_u32 v233, v233, 2, s2
	ds_read_b32 v74, v233
	v_subrev_u32_e32 v233, 0x53, v18
	v_and_b32_e32 v233, 0x7f, v233
	v_lshl_add_u32 v233, v233, 2, s2
	ds_read_b32 v75, v233
	s_waitcnt lgkmcnt(0)
	v_subrev_u32_e32 v233, 0x60, v18
	v_and_b32_e32 v233, 0x7f, v233
	v_lshl_add_u32 v233, v233, 2, s2
	ds_read_b32 v76, v233
	v_subrev_u32_e32 v233, 0x61, v18
	v_and_b32_e32 v233, 0x7f, v233
	v_lshl_add_u32 v233, v233, 2, s2
	ds_read_b32 v77, v233
	v_subrev_u32_e32 v233, 0x62, v18
	v_and_b32_e32 v233, 0x7f, v233
	v_lshl_add_u32 v233, v233, 2, s2
	ds_read_b32 v78, v233
	v_subrev_u32_e32 v233, 0x63, v18
	v_and_b32_e32 v233, 0x7f, v233
	v_lshl_add_u32 v233, v233, 2, s2
	ds_read_b32 v79, v233
	v_subrev_u32_e32 v233, 0x70, v18
	v_and_b32_e32 v233, 0x7f, v233
	v_lshl_add_u32 v233, v233, 2, s2
	ds_read_b32 v80, v233
	v_subrev_u32_e32 v233, 0x71, v18
	v_and_b32_e32 v233, 0x7f, v233
	v_lshl_add_u32 v233, v233, 2, s2
	ds_read_b32 v81, v233
	v_subrev_u32_e32 v233, 0x72, v18
	v_and_b32_e32 v233, 0x7f, v233
	v_lshl_add_u32 v233, v233, 2, s2
	ds_read_b32 v82, v233
	v_subrev_u32_e32 v233, 0x73, v18
	v_and_b32_e32 v233, 0x7f, v233
	v_lshl_add_u32 v233, v233, 2, s2
	ds_read_b32 v83, v233
	v_subrev_u32_e32 v233, 0x80, v18
	v_and_b32_e32 v233, 0x7f, v233
	v_lshl_add_u32 v233, v233, 2, s2
	ds_read_b32 v84, v233
	v_subrev_u32_e32 v233, 0x81, v18
	v_and_b32_e32 v233, 0x7f, v233
	v_lshl_add_u32 v233, v233, 2, s2
	ds_read_b32 v85, v233
	v_subrev_u32_e32 v233, 0x82, v18
	v_and_b32_e32 v233, 0x7f, v233
	v_lshl_add_u32 v233, v233, 2, s2
	ds_read_b32 v86, v233
	v_subrev_u32_e32 v233, 0x83, v18
	v_and_b32_e32 v233, 0x7f, v233
	v_lshl_add_u32 v233, v233, 2, s2
	ds_read_b32 v87, v233
	s_waitcnt lgkmcnt(0)
	s_waitcnt lgkmcnt(0)
	v_mov_b32_e32 v235, 0x80
	v_subrev_u32_e32 v233, 0, v18
	v_subrev_u32_e32 v234, 1, v18
	v_cmp_gt_u32_e32 vcc, 0x80, v233
	v_cmp_lt_u32_e64 s[6:7], v234, v235
	s_nop 0
	v_cndmask_b32_e32 v52, v89, v52, vcc
	v_cndmask_b32_e64 v53, v89, v53, s[6:7]
	v_subrev_u32_e32 v233, 2, v18
	v_subrev_u32_e32 v234, 3, v18
	v_cmp_gt_u32_e32 vcc, 0x80, v233
	v_cmp_lt_u32_e64 s[6:7], v234, v235
	s_nop 0
	v_cndmask_b32_e32 v54, v89, v54, vcc
	v_cndmask_b32_e64 v55, v89, v55, s[6:7]
	v_subrev_u32_e32 v233, 16, v18
	v_subrev_u32_e32 v234, 17, v18
	v_cmp_gt_u32_e32 vcc, 0x80, v233
	v_cmp_lt_u32_e64 s[6:7], v234, v235
	s_nop 0
	v_cndmask_b32_e32 v56, v89, v56, vcc
	v_cndmask_b32_e64 v57, v89, v57, s[6:7]
	v_subrev_u32_e32 v233, 18, v18
	v_subrev_u32_e32 v234, 19, v18
	v_cmp_gt_u32_e32 vcc, 0x80, v233
	v_cmp_lt_u32_e64 s[6:7], v234, v235
	s_nop 0
	v_cndmask_b32_e32 v58, v89, v58, vcc
	v_cndmask_b32_e64 v59, v89, v59, s[6:7]
	v_subrev_u32_e32 v233, 32, v18
	v_subrev_u32_e32 v234, 33, v18
	v_cmp_gt_u32_e32 vcc, 0x80, v233
	v_cmp_lt_u32_e64 s[6:7], v234, v235
	s_nop 0
	v_cndmask_b32_e32 v60, v89, v60, vcc
	v_cndmask_b32_e64 v61, v89, v61, s[6:7]
	v_subrev_u32_e32 v233, 34, v18
	v_subrev_u32_e32 v234, 35, v18
	v_cmp_gt_u32_e32 vcc, 0x80, v233
	v_cmp_lt_u32_e64 s[6:7], v234, v235
	s_nop 0
	v_cndmask_b32_e32 v62, v89, v62, vcc
	v_cndmask_b32_e64 v63, v89, v63, s[6:7]
	v_subrev_u32_e32 v233, 48, v18
	v_subrev_u32_e32 v234, 49, v18
	v_cmp_gt_u32_e32 vcc, 0x80, v233
	v_cmp_lt_u32_e64 s[6:7], v234, v235
	s_nop 0
	v_cndmask_b32_e32 v64, v89, v64, vcc
	v_cndmask_b32_e64 v65, v89, v65, s[6:7]
	v_subrev_u32_e32 v233, 50, v18
	v_subrev_u32_e32 v234, 51, v18
	v_cmp_gt_u32_e32 vcc, 0x80, v233
	v_cmp_lt_u32_e64 s[6:7], v234, v235
	s_nop 0
	v_cndmask_b32_e32 v66, v89, v66, vcc
	v_cndmask_b32_e64 v67, v89, v67, s[6:7]
	v_subrev_u32_e32 v233, 64, v18
	v_subrev_u32_e32 v234, 0x41, v18
	v_cmp_gt_u32_e32 vcc, 0x80, v233
	v_cmp_lt_u32_e64 s[6:7], v234, v235
	s_nop 0
	v_cndmask_b32_e32 v68, v89, v68, vcc
	v_cndmask_b32_e64 v69, v89, v69, s[6:7]
	v_subrev_u32_e32 v233, 0x42, v18
	v_subrev_u32_e32 v234, 0x43, v18
	v_cmp_gt_u32_e32 vcc, 0x80, v233
	v_cmp_lt_u32_e64 s[6:7], v234, v235
	s_nop 0
	v_cndmask_b32_e32 v70, v89, v70, vcc
	v_cndmask_b32_e64 v71, v89, v71, s[6:7]
	v_subrev_u32_e32 v233, 0x50, v18
	v_subrev_u32_e32 v234, 0x51, v18
	v_cmp_gt_u32_e32 vcc, 0x80, v233
	v_cmp_lt_u32_e64 s[6:7], v234, v235
	s_nop 0
	v_cndmask_b32_e32 v72, v89, v72, vcc
	v_cndmask_b32_e64 v73, v89, v73, s[6:7]
	v_subrev_u32_e32 v233, 0x52, v18
	v_subrev_u32_e32 v234, 0x53, v18
	v_cmp_gt_u32_e32 vcc, 0x80, v233
	v_cmp_lt_u32_e64 s[6:7], v234, v235
	s_nop 0
	v_cndmask_b32_e32 v74, v89, v74, vcc
	v_cndmask_b32_e64 v75, v89, v75, s[6:7]
	v_subrev_u32_e32 v233, 0x60, v18
	v_subrev_u32_e32 v234, 0x61, v18
	v_cmp_gt_u32_e32 vcc, 0x80, v233
	v_cmp_lt_u32_e64 s[6:7], v234, v235
	s_nop 0
	v_cndmask_b32_e32 v76, v89, v76, vcc
	v_cndmask_b32_e64 v77, v89, v77, s[6:7]
	v_subrev_u32_e32 v233, 0x62, v18
	v_subrev_u32_e32 v234, 0x63, v18
	v_cmp_gt_u32_e32 vcc, 0x80, v233
	v_cmp_lt_u32_e64 s[6:7], v234, v235
	s_nop 0
	v_cndmask_b32_e32 v78, v89, v78, vcc
	v_cndmask_b32_e64 v79, v89, v79, s[6:7]
	v_subrev_u32_e32 v233, 0x70, v18
	v_subrev_u32_e32 v234, 0x71, v18
	v_cmp_gt_u32_e32 vcc, 0x80, v233
	v_cmp_lt_u32_e64 s[6:7], v234, v235
	s_nop 0
	v_cndmask_b32_e32 v80, v89, v80, vcc
	v_cndmask_b32_e64 v81, v89, v81, s[6:7]
	v_subrev_u32_e32 v233, 0x72, v18
	v_subrev_u32_e32 v234, 0x73, v18
	v_cmp_gt_u32_e32 vcc, 0x80, v233
	v_cmp_lt_u32_e64 s[6:7], v234, v235
	s_nop 0
	v_cndmask_b32_e32 v82, v89, v82, vcc
	v_cndmask_b32_e64 v83, v89, v83, s[6:7]
	v_subrev_u32_e32 v233, 0x80, v18
	v_subrev_u32_e32 v234, 0x81, v18
	v_cmp_gt_u32_e32 vcc, 0x80, v233
	v_cmp_lt_u32_e64 s[6:7], v234, v235
	s_nop 0
	v_cndmask_b32_e32 v84, v89, v84, vcc
	v_cndmask_b32_e64 v85, v89, v85, s[6:7]
	v_subrev_u32_e32 v233, 0x82, v18
	v_subrev_u32_e32 v234, 0x83, v18
	v_cmp_gt_u32_e32 vcc, 0x80, v233
	v_cmp_lt_u32_e64 s[6:7], v234, v235
	s_nop 0
	v_cndmask_b32_e32 v86, v89, v86, vcc
	v_cndmask_b32_e64 v87, v89, v87, s[6:7]
.Lat_bzdone:
	s_add_u32 s48, s48, 0x14000
	s_addc_u32 s49, s49, 0
	ds_read_b128 v[160:163], v10 offset:0
	ds_read_b128 v[164:167], v10 offset:64
	ds_read_b128 v[168:171], v10 offset:2304
	ds_read_b128 v[172:175], v10 offset:2368
	ds_read_b128 v[176:179], v10 offset:4608
	ds_read_b128 v[180:183], v10 offset:4672
	ds_read_b128 v[184:187], v10 offset:6912
	ds_read_b128 v[188:191], v10 offset:6976
	ds_read_b128 v[192:195], v10 offset:9216
	ds_read_b128 v[196:199], v10 offset:9280
	s_waitcnt vmcnt(8)
	global_load_dwordx4 v[100:103], v8, s[48:49]
	global_load_dwordx4 v[104:107], v8, s[48:49] offset:64
	v_lshlrev_b32_e32 v234, 16, v92
	v_and_b32_e32 v235, 0xffff0000, v92
	v_pk_mul_f32 v[232:233], v[234:235], v[234:235]
	v_lshlrev_b32_e32 v234, 16, v93
	v_and_b32_e32 v235, 0xffff0000, v93
	v_pk_fma_f32 v[232:233], v[234:235], v[234:235], v[232:233]
	v_lshlrev_b32_e32 v234, 16, v94
	v_and_b32_e32 v235, 0xffff0000, v94
	v_pk_fma_f32 v[232:233], v[234:235], v[234:235], v[232:233]
	v_lshlrev_b32_e32 v234, 16, v95
	v_and_b32_e32 v235, 0xffff0000, v95
	v_pk_fma_f32 v[232:233], v[234:235], v[234:235], v[232:233]
	v_lshlrev_b32_e32 v234, 16, v96
	v_and_b32_e32 v235, 0xffff0000, v96
	v_pk_fma_f32 v[232:233], v[234:235], v[234:235], v[232:233]
	v_lshlrev_b32_e32 v234, 16, v97
	v_and_b32_e32 v235, 0xffff0000, v97
	v_pk_fma_f32 v[232:233], v[234:235], v[234:235], v[232:233]
	v_lshlrev_b32_e32 v234, 16, v98
	v_and_b32_e32 v235, 0xffff0000, v98
	v_pk_fma_f32 v[232:233], v[234:235], v[234:235], v[232:233]
	v_lshlrev_b32_e32 v234, 16, v99
	v_and_b32_e32 v235, 0xffff0000, v99
	v_pk_fma_f32 v[232:233], v[234:235], v[234:235], v[232:233]
	ds_read_b128 v[200:203], v10 offset:11520
	ds_read_b128 v[204:207], v10 offset:11584
	ds_read_b128 v[208:211], v10 offset:13824
	ds_read_b128 v[212:215], v10 offset:13888
	ds_read_b128 v[216:219], v10 offset:16128
	ds_read_b128 v[220:223], v10 offset:16192
	ds_read_b128 v[224:227], v10 offset:18432
	ds_read_b128 v[228:231], v10 offset:18496
	v_add_f32_e32 v232, v232, v233
	s_nop 0
	ds_bpermute_b32 v233, v15, v232
	s_waitcnt lgkmcnt(9)
	v_mfma_f32_16x16x32_bf16 v[108:111], v[160:163], v[92:95], 0
	v_mfma_f32_16x16x32_bf16 v[112:115], v[168:171], v[92:95], 0
	v_mfma_f32_16x16x32_bf16 v[116:119], v[176:179], v[92:95], 0
	v_mfma_f32_16x16x32_bf16 v[120:123], v[184:187], v[92:95], 0
	v_mfma_f32_16x16x32_bf16 v[124:127], v[192:195], v[92:95], 0
	v_mfma_f32_16x16x32_bf16 v[108:111], v[164:167], v[96:99], v[108:111]
	v_mfma_f32_16x16x32_bf16 v[112:115], v[172:175], v[96:99], v[112:115]
	v_mfma_f32_16x16x32_bf16 v[116:119], v[180:183], v[96:99], v[116:119]
	v_mfma_f32_16x16x32_bf16 v[120:123], v[188:191], v[96:99], v[120:123]
	v_mfma_f32_16x16x32_bf16 v[124:127], v[196:199], v[96:99], v[124:127]
	s_waitcnt lgkmcnt(0)
	v_add_f32_e32 v232, v232, v233
	v_mfma_f32_16x16x32_bf16 v[128:131], v[200:203], v[92:95], 0
	v_mfma_f32_16x16x32_bf16 v[132:135], v[208:211], v[92:95], 0
	v_mfma_f32_16x16x32_bf16 v[136:139], v[216:219], v[92:95], 0
	v_mfma_f32_16x16x32_bf16 v[140:143], v[224:227], v[92:95], 0
	ds_bpermute_b32 v233, v16, v232
	v_mfma_f32_16x16x32_bf16 v[128:131], v[204:207], v[96:99], v[128:131]
	v_mfma_f32_16x16x32_bf16 v[132:135], v[212:215], v[96:99], v[132:135]
	v_mfma_f32_16x16x32_bf16 v[136:139], v[220:223], v[96:99], v[136:139]
	v_mfma_f32_16x16x32_bf16 v[140:143], v[228:231], v[96:99], v[140:143]
	ds_read2_b64 v[160:163], v11 offset0:0 offset1:4
	ds_read2_b64 v[164:167], v12 offset0:0 offset1:4
	ds_read2_b64 v[168:171], v13 offset0:0 offset1:4
	ds_read2_b64 v[172:175], v14 offset0:0 offset1:4
	ds_read2_b64 v[176:179], v11 offset0:8 offset1:12
	ds_read2_b64 v[180:183], v12 offset0:8 offset1:12
	ds_read2_b64 v[184:187], v13 offset0:8 offset1:12
	ds_read2_b64 v[188:191], v14 offset0:8 offset1:12
	ds_read2_b64 v[192:195], v11 offset0:16 offset1:20
	ds_read2_b64 v[196:199], v12 offset0:16 offset1:20
	ds_read2_b64 v[200:203], v13 offset0:16 offset1:20
	ds_read2_b64 v[204:207], v14 offset0:16 offset1:20
	s_waitcnt lgkmcnt(12)
	v_add_f32_e32 v232, v232, v233
	v_mul_f32_e32 v232, 0x3c800000, v232
	v_add_f32_e32 v232, 0x358637bd, v232
	v_rsq_f32_e32 v236, v232
	s_nop 0
	v_mov_b32_e32 v237, v236
	s_nop 1
	v_pk_fma_f32 v[108:109], v[108:109], v[236:237], v[52:53]
	v_pk_fma_f32 v[110:111], v[110:111], v[236:237], v[54:55]
	v_pk_fma_f32 v[112:113], v[112:113], v[236:237], v[56:57]
	v_pk_fma_f32 v[114:115], v[114:115], v[236:237], v[58:59]
	v_pk_fma_f32 v[116:117], v[116:117], v[236:237], v[60:61]
	v_pk_fma_f32 v[118:119], v[118:119], v[236:237], v[62:63]
	v_pk_fma_f32 v[120:121], v[120:121], v[236:237], v[64:65]
	v_pk_fma_f32 v[122:123], v[122:123], v[236:237], v[66:67]
	v_pk_fma_f32 v[124:125], v[124:125], v[236:237], v[68:69]
	v_pk_fma_f32 v[126:127], v[126:127], v[236:237], v[70:71]
	v_pk_fma_f32 v[128:129], v[128:129], v[236:237], v[72:73]
	v_pk_fma_f32 v[130:131], v[130:131], v[236:237], v[74:75]
	v_pk_fma_f32 v[132:133], v[132:133], v[236:237], v[76:77]
	v_pk_fma_f32 v[134:135], v[134:135], v[236:237], v[78:79]
	v_pk_fma_f32 v[136:137], v[136:137], v[236:237], v[80:81]
	v_pk_fma_f32 v[138:139], v[138:139], v[236:237], v[82:83]
	v_pk_fma_f32 v[140:141], v[140:141], v[236:237], v[84:85]
	v_pk_fma_f32 v[142:143], v[142:143], v[236:237], v[86:87]
	v_exp_f32_e32 v108, v108
	v_exp_f32_e32 v109, v109
	v_exp_f32_e32 v110, v110
	v_exp_f32_e32 v111, v111
	v_exp_f32_e32 v112, v112
	v_exp_f32_e32 v113, v113
	v_exp_f32_e32 v114, v114
	v_exp_f32_e32 v115, v115
	v_exp_f32_e32 v116, v116
	v_exp_f32_e32 v117, v117
	v_exp_f32_e32 v118, v118
	v_exp_f32_e32 v119, v119
	v_exp_f32_e32 v120, v120
	v_exp_f32_e32 v121, v121
	v_exp_f32_e32 v122, v122
	v_exp_f32_e32 v123, v123
	v_exp_f32_e32 v124, v124
	v_exp_f32_e32 v125, v125
	v_exp_f32_e32 v126, v126
	v_exp_f32_e32 v127, v127
	v_exp_f32_e32 v128, v128
	v_exp_f32_e32 v129, v129
	v_exp_f32_e32 v130, v130
	v_exp_f32_e32 v131, v131
	v_exp_f32_e32 v132, v132
	v_exp_f32_e32 v133, v133
	v_exp_f32_e32 v134, v134
	v_exp_f32_e32 v135, v135
	v_exp_f32_e32 v136, v136
	v_exp_f32_e32 v137, v137
	v_exp_f32_e32 v138, v138
	v_exp_f32_e32 v139, v139
	v_exp_f32_e32 v140, v140
	v_exp_f32_e32 v141, v141
	v_exp_f32_e32 v142, v142
	v_exp_f32_e32 v143, v143
	s_cmp_lg_u32 s36, 0
	s_cbranch_scc1 .Lat_m0
	v_mov_b32_e32 v108, 0
	v_mov_b32_e32 v109, 0
	v_mov_b32_e32 v110, 0
	v_mov_b32_e32 v111, 0
	v_mov_b32_e32 v112, 0
	v_mov_b32_e32 v113, 0
	v_mov_b32_e32 v114, 0
	v_mov_b32_e32 v115, 0
	v_mov_b32_e32 v116, 0
	v_mov_b32_e32 v117, 0
	v_mov_b32_e32 v118, 0
	v_mov_b32_e32 v119, 0
	v_mov_b32_e32 v120, 0
	v_mov_b32_e32 v121, 0
	v_mov_b32_e32 v122, 0
	v_mov_b32_e32 v123, 0
	v_mov_b32_e32 v124, 0
	v_mov_b32_e32 v125, 0
	v_mov_b32_e32 v126, 0
	v_mov_b32_e32 v127, 0
	v_mov_b32_e32 v128, 0
	v_mov_b32_e32 v129, 0
	v_mov_b32_e32 v130, 0
	v_mov_b32_e32 v131, 0
	v_mov_b32_e32 v132, 0
	v_mov_b32_e32 v133, 0
	v_mov_b32_e32 v134, 0
	v_mov_b32_e32 v135, 0
	v_mov_b32_e32 v136, 0
	v_mov_b32_e32 v137, 0
	v_mov_b32_e32 v138, 0
	v_mov_b32_e32 v139, 0
.Lat_m0:
	s_nop 0
	v_pk_add_f32 v[232:233], v[108:109], v[110:111]
	v_pk_add_f32 v[234:235], v[112:113], v[114:115]
	v_pk_add_f32 v[232:233], v[232:233], v[116:117]
	v_pk_add_f32 v[234:235], v[234:235], v[118:119]
	v_pk_add_f32 v[232:233], v[232:233], v[120:121]
	v_pk_add_f32 v[234:235], v[234:235], v[122:123]
	v_pk_add_f32 v[232:233], v[232:233], v[124:125]
	v_pk_add_f32 v[234:235], v[234:235], v[126:127]
	v_pk_add_f32 v[232:233], v[232:233], v[128:129]
	v_pk_add_f32 v[234:235], v[234:235], v[130:131]
	v_pk_add_f32 v[232:233], v[232:233], v[132:133]
	v_pk_add_f32 v[234:235], v[234:235], v[134:135]
	v_pk_add_f32 v[232:233], v[232:233], v[136:137]
	v_pk_add_f32 v[234:235], v[234:235], v[138:139]
	v_pk_add_f32 v[232:233], v[232:233], v[140:141]
	v_pk_add_f32 v[234:235], v[234:235], v[142:143]
	v_pk_add_f32 v[232:233], v[232:233], v[234:235]
	s_nop 0
	v_add_f32_e32 v232, v232, v233
	v_cvt_pk_bf16_f32 v108, v108, v109
	v_cvt_pk_bf16_f32 v109, v110, v111
	v_cvt_pk_bf16_f32 v110, v112, v113
	v_cvt_pk_bf16_f32 v111, v114, v115
	v_cvt_pk_bf16_f32 v116, v116, v117
	v_cvt_pk_bf16_f32 v117, v118, v119
	v_cvt_pk_bf16_f32 v118, v120, v121
	v_cvt_pk_bf16_f32 v119, v122, v123
	v_cvt_pk_bf16_f32 v124, v124, v125
	v_cvt_pk_bf16_f32 v125, v126, v127
	v_cvt_pk_bf16_f32 v126, v128, v129
	v_cvt_pk_bf16_f32 v127, v130, v131
	v_cvt_pk_bf16_f32 v132, v132, v133
	v_cvt_pk_bf16_f32 v133, v134, v135
	v_cvt_pk_bf16_f32 v134, v136, v137
	v_cvt_pk_bf16_f32 v135, v138, v139
	v_cvt_pk_bf16_f32 v140, v140, v141
	v_cvt_pk_bf16_f32 v141, v142, v143
	v_mov_b32_e32 v142, 0
	v_mov_b32_e32 v143, 0
	ds_bpermute_b32 v233, v15, v232
	s_waitcnt lgkmcnt(1)
	v_mfma_f32_16x16x32_bf16 v[144:147], v[160:163], v[108:111], 0
	v_mfma_f32_16x16x32_bf16 v[148:151], v[164:167], v[108:111], 0
	v_mfma_f32_16x16x32_bf16 v[152:155], v[168:171], v[108:111], 0
	v_mfma_f32_16x16x32_bf16 v[156:159], v[172:175], v[108:111], 0
	v_mfma_f32_16x16x32_bf16 v[144:147], v[176:179], v[116:119], v[144:147]
	v_mfma_f32_16x16x32_bf16 v[148:151], v[180:183], v[116:119], v[148:151]
	v_mfma_f32_16x16x32_bf16 v[152:155], v[184:187], v[116:119], v[152:155]
	v_mfma_f32_16x16x32_bf16 v[156:159], v[188:191], v[116:119], v[156:159]
	v_mfma_f32_16x16x32_bf16 v[144:147], v[192:195], v[124:127], v[144:147]
	v_mfma_f32_16x16x32_bf16 v[148:151], v[196:199], v[124:127], v[148:151]
	v_mfma_f32_16x16x32_bf16 v[152:155], v[200:203], v[124:127], v[152:155]
	v_mfma_f32_16x16x32_bf16 v[156:159], v[204:207], v[124:127], v[156:159]
	ds_read2_b64 v[160:163], v11 offset0:24 offset1:28
	ds_read2_b64 v[164:167], v12 offset0:24 offset1:28
	ds_read2_b64 v[168:171], v13 offset0:24 offset1:28
	ds_read2_b64 v[172:175], v14 offset0:24 offset1:28
	ds_read2_b64 v[176:179], v11 offset0:32 offset1:32
	ds_read2_b64 v[180:183], v12 offset0:32 offset1:32
	ds_read2_b64 v[184:187], v13 offset0:32 offset1:32
	ds_read2_b64 v[188:191], v14 offset0:32 offset1:32
	s_waitcnt lgkmcnt(8)
	v_add_f32_e32 v232, v232, v233
	s_nop 0
	ds_bpermute_b32 v233, v16, v232
	s_waitcnt lgkmcnt(1)
	v_mfma_f32_16x16x32_bf16 v[144:147], v[160:163], v[132:135], v[144:147]
	v_mfma_f32_16x16x32_bf16 v[148:151], v[164:167], v[132:135], v[148:151]
	v_mfma_f32_16x16x32_bf16 v[152:155], v[168:171], v[132:135], v[152:155]
	v_mfma_f32_16x16x32_bf16 v[156:159], v[172:175], v[132:135], v[156:159]
	v_mfma_f32_16x16x32_bf16 v[144:147], v[176:179], v[140:143], v[144:147]
	v_mfma_f32_16x16x32_bf16 v[148:151], v[180:183], v[140:143], v[148:151]
	v_mfma_f32_16x16x32_bf16 v[152:155], v[184:187], v[140:143], v[152:155]
	v_mfma_f32_16x16x32_bf16 v[156:159], v[188:191], v[140:143], v[156:159]
	s_waitcnt lgkmcnt(0)
	v_add_f32_e32 v232, v232, v233
	v_add_f32_e32 v232, v232, v88
	v_rcp_f32_e32 v236, v232
	s_nop 0
	v_mov_b32_e32 v237, v236
	s_nop 4
	v_pk_mul_f32 v[144:145], v[144:145], v[236:237]
	v_pk_mul_f32 v[146:147], v[146:147], v[236:237]
	v_pk_mul_f32 v[148:149], v[148:149], v[236:237]
	v_pk_mul_f32 v[150:151], v[150:151], v[236:237]
	v_pk_mul_f32 v[152:153], v[152:153], v[236:237]
	v_pk_mul_f32 v[154:155], v[154:155], v[236:237]
	v_pk_mul_f32 v[156:157], v[156:157], v[236:237]
	v_pk_mul_f32 v[158:159], v[158:159], v[236:237]
	v_cvt_pk_bf16_f32 v144, v144, v145
	v_cvt_pk_bf16_f32 v145, v146, v147
	v_cvt_pk_bf16_f32 v148, v148, v149
	v_cvt_pk_bf16_f32 v149, v150, v151
	v_cvt_pk_bf16_f32 v152, v152, v153
	v_cvt_pk_bf16_f32 v153, v154, v155
	v_cvt_pk_bf16_f32 v156, v156, v157
	v_cvt_pk_bf16_f32 v157, v158, v159
	global_store_dwordx2 v9, v[144:145], s[50:51] offset:0
	global_store_dwordx2 v9, v[148:149], s[50:51] offset:32
	global_store_dwordx2 v9, v[152:153], s[50:51] offset:64
	global_store_dwordx2 v9, v[156:157], s[50:51] offset:96
	s_add_u32 s50, s50, 0x10000
	s_addc_u32 s51, s51, 0
	s_add_u32 s48, s48, 0x14000
	s_addc_u32 s49, s49, 0
	ds_read_b128 v[160:163], v10 offset:2304
	ds_read_b128 v[164:167], v10 offset:2368
	ds_read_b128 v[168:171], v10 offset:4608
	ds_read_b128 v[172:175], v10 offset:4672
	ds_read_b128 v[176:179], v10 offset:6912
	ds_read_b128 v[180:183], v10 offset:6976
	ds_read_b128 v[184:187], v10 offset:9216
	ds_read_b128 v[188:191], v10 offset:9280
	ds_read_b128 v[192:195], v10 offset:11520
	ds_read_b128 v[196:199], v10 offset:11584
	s_waitcnt vmcnt(4)
	global_load_dwordx4 v[92:95], v8, s[48:49]
	global_load_dwordx4 v[96:99], v8, s[48:49] offset:64
	v_lshlrev_b32_e32 v234, 16, v100
	v_and_b32_e32 v235, 0xffff0000, v100
	v_pk_mul_f32 v[232:233], v[234:235], v[234:235]
	v_lshlrev_b32_e32 v234, 16, v101
	v_and_b32_e32 v235, 0xffff0000, v101
	v_pk_fma_f32 v[232:233], v[234:235], v[234:235], v[232:233]
	v_lshlrev_b32_e32 v234, 16, v102
	v_and_b32_e32 v235, 0xffff0000, v102
	v_pk_fma_f32 v[232:233], v[234:235], v[234:235], v[232:233]
	v_lshlrev_b32_e32 v234, 16, v103
	v_and_b32_e32 v235, 0xffff0000, v103
	v_pk_fma_f32 v[232:233], v[234:235], v[234:235], v[232:233]
	v_lshlrev_b32_e32 v234, 16, v104
	v_and_b32_e32 v235, 0xffff0000, v104
	v_pk_fma_f32 v[232:233], v[234:235], v[234:235], v[232:233]
	v_lshlrev_b32_e32 v234, 16, v105
	v_and_b32_e32 v235, 0xffff0000, v105
	v_pk_fma_f32 v[232:233], v[234:235], v[234:235], v[232:233]
	v_lshlrev_b32_e32 v234, 16, v106
	v_and_b32_e32 v235, 0xffff0000, v106
	v_pk_fma_f32 v[232:233], v[234:235], v[234:235], v[232:233]
	v_lshlrev_b32_e32 v234, 16, v107
	v_and_b32_e32 v235, 0xffff0000, v107
	v_pk_fma_f32 v[232:233], v[234:235], v[234:235], v[232:233]
	ds_read_b128 v[200:203], v10 offset:13824
	ds_read_b128 v[204:207], v10 offset:13888
	ds_read_b128 v[208:211], v10 offset:16128
	ds_read_b128 v[212:215], v10 offset:16192
	ds_read_b128 v[216:219], v10 offset:18432
	ds_read_b128 v[220:223], v10 offset:18496
	ds_read_b128 v[224:227], v10 offset:20736
	ds_read_b128 v[228:231], v10 offset:20800
	v_add_f32_e32 v232, v232, v233
	s_nop 0
	ds_bpermute_b32 v233, v15, v232
	s_waitcnt lgkmcnt(9)
	v_mfma_f32_16x16x32_bf16 v[108:111], v[160:163], v[100:103], 0
	v_mfma_f32_16x16x32_bf16 v[112:115], v[168:171], v[100:103], 0
	v_mfma_f32_16x16x32_bf16 v[116:119], v[176:179], v[100:103], 0
	v_mfma_f32_16x16x32_bf16 v[120:123], v[184:187], v[100:103], 0
	v_mfma_f32_16x16x32_bf16 v[124:127], v[192:195], v[100:103], 0
	v_mfma_f32_16x16x32_bf16 v[108:111], v[164:167], v[104:107], v[108:111]
	v_mfma_f32_16x16x32_bf16 v[112:115], v[172:175], v[104:107], v[112:115]
	v_mfma_f32_16x16x32_bf16 v[116:119], v[180:183], v[104:107], v[116:119]
	v_mfma_f32_16x16x32_bf16 v[120:123], v[188:191], v[104:107], v[120:123]
	v_mfma_f32_16x16x32_bf16 v[124:127], v[196:199], v[104:107], v[124:127]
	s_waitcnt lgkmcnt(0)
	v_add_f32_e32 v232, v232, v233
	v_mfma_f32_16x16x32_bf16 v[128:131], v[200:203], v[100:103], 0
	v_mfma_f32_16x16x32_bf16 v[132:135], v[208:211], v[100:103], 0
	v_mfma_f32_16x16x32_bf16 v[136:139], v[216:219], v[100:103], 0
	v_mfma_f32_16x16x32_bf16 v[140:143], v[224:227], v[100:103], 0
	ds_bpermute_b32 v233, v16, v232
	v_mfma_f32_16x16x32_bf16 v[128:131], v[204:207], v[104:107], v[128:131]
	v_mfma_f32_16x16x32_bf16 v[132:135], v[212:215], v[104:107], v[132:135]
	v_mfma_f32_16x16x32_bf16 v[136:139], v[220:223], v[104:107], v[136:139]
	v_mfma_f32_16x16x32_bf16 v[140:143], v[228:231], v[104:107], v[140:143]
	ds_read2_b64 v[160:163], v11 offset0:4 offset1:8
	ds_read2_b64 v[164:167], v12 offset0:4 offset1:8
	ds_read2_b64 v[168:171], v13 offset0:4 offset1:8
	ds_read2_b64 v[172:175], v14 offset0:4 offset1:8
	ds_read2_b64 v[176:179], v11 offset0:12 offset1:16
	ds_read2_b64 v[180:183], v12 offset0:12 offset1:16
	ds_read2_b64 v[184:187], v13 offset0:12 offset1:16
	ds_read2_b64 v[188:191], v14 offset0:12 offset1:16
	ds_read2_b64 v[192:195], v11 offset0:20 offset1:24
	ds_read2_b64 v[196:199], v12 offset0:20 offset1:24
	ds_read2_b64 v[200:203], v13 offset0:20 offset1:24
	ds_read2_b64 v[204:207], v14 offset0:20 offset1:24
	s_waitcnt lgkmcnt(12)
	v_add_f32_e32 v232, v232, v233
	v_mul_f32_e32 v232, 0x3c800000, v232
	v_add_f32_e32 v232, 0x358637bd, v232
	v_rsq_f32_e32 v236, v232
	s_nop 0
	v_mov_b32_e32 v237, v236
	s_nop 1
	v_pk_fma_f32 v[108:109], v[108:109], v[236:237], v[52:53]
	v_pk_fma_f32 v[110:111], v[110:111], v[236:237], v[54:55]
	v_pk_fma_f32 v[112:113], v[112:113], v[236:237], v[56:57]
	v_pk_fma_f32 v[114:115], v[114:115], v[236:237], v[58:59]
	v_pk_fma_f32 v[116:117], v[116:117], v[236:237], v[60:61]
	v_pk_fma_f32 v[118:119], v[118:119], v[236:237], v[62:63]
	v_pk_fma_f32 v[120:121], v[120:121], v[236:237], v[64:65]
	v_pk_fma_f32 v[122:123], v[122:123], v[236:237], v[66:67]
	v_pk_fma_f32 v[124:125], v[124:125], v[236:237], v[68:69]
	v_pk_fma_f32 v[126:127], v[126:127], v[236:237], v[70:71]
	v_pk_fma_f32 v[128:129], v[128:129], v[236:237], v[72:73]
	v_pk_fma_f32 v[130:131], v[130:131], v[236:237], v[74:75]
	v_pk_fma_f32 v[132:133], v[132:133], v[236:237], v[76:77]
	v_pk_fma_f32 v[134:135], v[134:135], v[236:237], v[78:79]
	v_pk_fma_f32 v[136:137], v[136:137], v[236:237], v[80:81]
	v_pk_fma_f32 v[138:139], v[138:139], v[236:237], v[82:83]
	v_pk_fma_f32 v[140:141], v[140:141], v[236:237], v[84:85]
	v_pk_fma_f32 v[142:143], v[142:143], v[236:237], v[86:87]
	v_exp_f32_e32 v108, v108
	v_exp_f32_e32 v109, v109
	v_exp_f32_e32 v110, v110
	v_exp_f32_e32 v111, v111
	v_exp_f32_e32 v112, v112
	v_exp_f32_e32 v113, v113
	v_exp_f32_e32 v114, v114
	v_exp_f32_e32 v115, v115
	v_exp_f32_e32 v116, v116
	v_exp_f32_e32 v117, v117
	v_exp_f32_e32 v118, v118
	v_exp_f32_e32 v119, v119
	v_exp_f32_e32 v120, v120
	v_exp_f32_e32 v121, v121
	v_exp_f32_e32 v122, v122
	v_exp_f32_e32 v123, v123
	v_exp_f32_e32 v124, v124
	v_exp_f32_e32 v125, v125
	v_exp_f32_e32 v126, v126
	v_exp_f32_e32 v127, v127
	v_exp_f32_e32 v128, v128
	v_exp_f32_e32 v129, v129
	v_exp_f32_e32 v130, v130
	v_exp_f32_e32 v131, v131
	v_exp_f32_e32 v132, v132
	v_exp_f32_e32 v133, v133
	v_exp_f32_e32 v134, v134
	v_exp_f32_e32 v135, v135
	v_exp_f32_e32 v136, v136
	v_exp_f32_e32 v137, v137
	v_exp_f32_e32 v138, v138
	v_exp_f32_e32 v139, v139
	v_exp_f32_e32 v140, v140
	v_exp_f32_e32 v141, v141
	v_exp_f32_e32 v142, v142
	v_exp_f32_e32 v143, v143
	s_cmp_lg_u32 s36, 0
	s_cbranch_scc1 .Lat_m1
	v_mov_b32_e32 v108, 0
	v_mov_b32_e32 v109, 0
	v_mov_b32_e32 v110, 0
	v_mov_b32_e32 v111, 0
	v_mov_b32_e32 v112, 0
	v_mov_b32_e32 v113, 0
	v_mov_b32_e32 v114, 0
	v_mov_b32_e32 v115, 0
	v_mov_b32_e32 v116, 0
	v_mov_b32_e32 v117, 0
	v_mov_b32_e32 v118, 0
	v_mov_b32_e32 v119, 0
	v_mov_b32_e32 v120, 0
	v_mov_b32_e32 v121, 0
	v_mov_b32_e32 v122, 0
	v_mov_b32_e32 v123, 0
	v_mov_b32_e32 v124, 0
	v_mov_b32_e32 v125, 0
	v_mov_b32_e32 v126, 0
	v_mov_b32_e32 v127, 0
	v_mov_b32_e32 v128, 0
	v_mov_b32_e32 v129, 0
	v_mov_b32_e32 v130, 0
	v_mov_b32_e32 v131, 0
	v_mov_b32_e32 v132, 0
	v_mov_b32_e32 v133, 0
	v_mov_b32_e32 v134, 0
	v_mov_b32_e32 v135, 0
.Lat_m1:
	s_nop 0
	v_pk_add_f32 v[232:233], v[108:109], v[110:111]
	v_pk_add_f32 v[234:235], v[112:113], v[114:115]
	v_pk_add_f32 v[232:233], v[232:233], v[116:117]
	v_pk_add_f32 v[234:235], v[234:235], v[118:119]
	v_pk_add_f32 v[232:233], v[232:233], v[120:121]
	v_pk_add_f32 v[234:235], v[234:235], v[122:123]
	v_pk_add_f32 v[232:233], v[232:233], v[124:125]
	v_pk_add_f32 v[234:235], v[234:235], v[126:127]
	v_pk_add_f32 v[232:233], v[232:233], v[128:129]
	v_pk_add_f32 v[234:235], v[234:235], v[130:131]
	v_pk_add_f32 v[232:233], v[232:233], v[132:133]
	v_pk_add_f32 v[234:235], v[234:235], v[134:135]
	v_pk_add_f32 v[232:233], v[232:233], v[136:137]
	v_pk_add_f32 v[234:235], v[234:235], v[138:139]
	v_pk_add_f32 v[232:233], v[232:233], v[140:141]
	v_pk_add_f32 v[234:235], v[234:235], v[142:143]
	v_pk_add_f32 v[232:233], v[232:233], v[234:235]
	s_nop 0
	v_add_f32_e32 v232, v232, v233
	v_cvt_pk_bf16_f32 v108, v108, v109
	v_cvt_pk_bf16_f32 v109, v110, v111
	v_cvt_pk_bf16_f32 v110, v112, v113
	v_cvt_pk_bf16_f32 v111, v114, v115
	v_cvt_pk_bf16_f32 v116, v116, v117
	v_cvt_pk_bf16_f32 v117, v118, v119
	v_cvt_pk_bf16_f32 v118, v120, v121
	v_cvt_pk_bf16_f32 v119, v122, v123
	v_cvt_pk_bf16_f32 v124, v124, v125
	v_cvt_pk_bf16_f32 v125, v126, v127
	v_cvt_pk_bf16_f32 v126, v128, v129
	v_cvt_pk_bf16_f32 v127, v130, v131
	v_cvt_pk_bf16_f32 v132, v132, v133
	v_cvt_pk_bf16_f32 v133, v134, v135
	v_cvt_pk_bf16_f32 v134, v136, v137
	v_cvt_pk_bf16_f32 v135, v138, v139
	v_cvt_pk_bf16_f32 v140, v140, v141
	v_cvt_pk_bf16_f32 v141, v142, v143
	v_mov_b32_e32 v142, 0
	v_mov_b32_e32 v143, 0
	ds_bpermute_b32 v233, v15, v232
	s_waitcnt lgkmcnt(1)
	v_mfma_f32_16x16x32_bf16 v[144:147], v[160:163], v[108:111], 0
	v_mfma_f32_16x16x32_bf16 v[148:151], v[164:167], v[108:111], 0
	v_mfma_f32_16x16x32_bf16 v[152:155], v[168:171], v[108:111], 0
	v_mfma_f32_16x16x32_bf16 v[156:159], v[172:175], v[108:111], 0
	v_mfma_f32_16x16x32_bf16 v[144:147], v[176:179], v[116:119], v[144:147]
	v_mfma_f32_16x16x32_bf16 v[148:151], v[180:183], v[116:119], v[148:151]
	v_mfma_f32_16x16x32_bf16 v[152:155], v[184:187], v[116:119], v[152:155]
	v_mfma_f32_16x16x32_bf16 v[156:159], v[188:191], v[116:119], v[156:159]
	v_mfma_f32_16x16x32_bf16 v[144:147], v[192:195], v[124:127], v[144:147]
	v_mfma_f32_16x16x32_bf16 v[148:151], v[196:199], v[124:127], v[148:151]
	v_mfma_f32_16x16x32_bf16 v[152:155], v[200:203], v[124:127], v[152:155]
	v_mfma_f32_16x16x32_bf16 v[156:159], v[204:207], v[124:127], v[156:159]
	ds_read2_b64 v[160:163], v11 offset0:28 offset1:32
	ds_read2_b64 v[164:167], v12 offset0:28 offset1:32
	ds_read2_b64 v[168:171], v13 offset0:28 offset1:32
	ds_read2_b64 v[172:175], v14 offset0:28 offset1:32
	ds_read2_b64 v[176:179], v11 offset0:36 offset1:36
	ds_read2_b64 v[180:183], v12 offset0:36 offset1:36
	ds_read2_b64 v[184:187], v13 offset0:36 offset1:36
	ds_read2_b64 v[188:191], v14 offset0:36 offset1:36
	s_waitcnt lgkmcnt(8)
	v_add_f32_e32 v232, v232, v233
	s_nop 0
	ds_bpermute_b32 v233, v16, v232
	s_waitcnt lgkmcnt(1)
	v_mfma_f32_16x16x32_bf16 v[144:147], v[160:163], v[132:135], v[144:147]
	v_mfma_f32_16x16x32_bf16 v[148:151], v[164:167], v[132:135], v[148:151]
	v_mfma_f32_16x16x32_bf16 v[152:155], v[168:171], v[132:135], v[152:155]
	v_mfma_f32_16x16x32_bf16 v[156:159], v[172:175], v[132:135], v[156:159]
	v_mfma_f32_16x16x32_bf16 v[144:147], v[176:179], v[140:143], v[144:147]
	v_mfma_f32_16x16x32_bf16 v[148:151], v[180:183], v[140:143], v[148:151]
	v_mfma_f32_16x16x32_bf16 v[152:155], v[184:187], v[140:143], v[152:155]
	v_mfma_f32_16x16x32_bf16 v[156:159], v[188:191], v[140:143], v[156:159]
	s_waitcnt lgkmcnt(0)
	v_add_f32_e32 v232, v232, v233
	v_add_f32_e32 v232, v232, v88
	v_rcp_f32_e32 v236, v232
	s_nop 0
	v_mov_b32_e32 v237, v236
	s_nop 4
	v_pk_mul_f32 v[144:145], v[144:145], v[236:237]
	v_pk_mul_f32 v[146:147], v[146:147], v[236:237]
	v_pk_mul_f32 v[148:149], v[148:149], v[236:237]
	v_pk_mul_f32 v[150:151], v[150:151], v[236:237]
	v_pk_mul_f32 v[152:153], v[152:153], v[236:237]
	v_pk_mul_f32 v[154:155], v[154:155], v[236:237]
	v_pk_mul_f32 v[156:157], v[156:157], v[236:237]
	v_pk_mul_f32 v[158:159], v[158:159], v[236:237]
	v_cvt_pk_bf16_f32 v144, v144, v145
	v_cvt_pk_bf16_f32 v145, v146, v147
	v_cvt_pk_bf16_f32 v148, v148, v149
	v_cvt_pk_bf16_f32 v149, v150, v151
	v_cvt_pk_bf16_f32 v152, v152, v153
	v_cvt_pk_bf16_f32 v153, v154, v155
	v_cvt_pk_bf16_f32 v156, v156, v157
	v_cvt_pk_bf16_f32 v157, v158, v159
	global_store_dwordx2 v9, v[144:145], s[50:51] offset:0
	global_store_dwordx2 v9, v[148:149], s[50:51] offset:32
	global_store_dwordx2 v9, v[152:153], s[50:51] offset:64
	global_store_dwordx2 v9, v[156:157], s[50:51] offset:96
	s_add_u32 s50, s50, 0x10000
	s_addc_u32 s51, s51, 0
	s_add_u32 s48, s48, 0x14000
	s_addc_u32 s49, s49, 0
	ds_read_b128 v[160:163], v10 offset:4608
	ds_read_b128 v[164:167], v10 offset:4672
	ds_read_b128 v[168:171], v10 offset:6912
	ds_read_b128 v[172:175], v10 offset:6976
	ds_read_b128 v[176:179], v10 offset:9216
	ds_read_b128 v[180:183], v10 offset:9280
	ds_read_b128 v[184:187], v10 offset:11520
	ds_read_b128 v[188:191], v10 offset:11584
	ds_read_b128 v[192:195], v10 offset:13824
	ds_read_b128 v[196:199], v10 offset:13888
	s_waitcnt vmcnt(4)
	global_load_dwordx4 v[100:103], v8, s[48:49]
	global_load_dwordx4 v[104:107], v8, s[48:49] offset:64
	v_lshlrev_b32_e32 v234, 16, v92
	v_and_b32_e32 v235, 0xffff0000, v92
	v_pk_mul_f32 v[232:233], v[234:235], v[234:235]
	v_lshlrev_b32_e32 v234, 16, v93
	v_and_b32_e32 v235, 0xffff0000, v93
	v_pk_fma_f32 v[232:233], v[234:235], v[234:235], v[232:233]
	v_lshlrev_b32_e32 v234, 16, v94
	v_and_b32_e32 v235, 0xffff0000, v94
	v_pk_fma_f32 v[232:233], v[234:235], v[234:235], v[232:233]
	v_lshlrev_b32_e32 v234, 16, v95
	v_and_b32_e32 v235, 0xffff0000, v95
	v_pk_fma_f32 v[232:233], v[234:235], v[234:235], v[232:233]
	v_lshlrev_b32_e32 v234, 16, v96
	v_and_b32_e32 v235, 0xffff0000, v96
	v_pk_fma_f32 v[232:233], v[234:235], v[234:235], v[232:233]
	v_lshlrev_b32_e32 v234, 16, v97
	v_and_b32_e32 v235, 0xffff0000, v97
	v_pk_fma_f32 v[232:233], v[234:235], v[234:235], v[232:233]
	v_lshlrev_b32_e32 v234, 16, v98
	v_and_b32_e32 v235, 0xffff0000, v98
	v_pk_fma_f32 v[232:233], v[234:235], v[234:235], v[232:233]
	v_lshlrev_b32_e32 v234, 16, v99
	v_and_b32_e32 v235, 0xffff0000, v99
	v_pk_fma_f32 v[232:233], v[234:235], v[234:235], v[232:233]
	ds_read_b128 v[200:203], v10 offset:16128
	ds_read_b128 v[204:207], v10 offset:16192
	ds_read_b128 v[208:211], v10 offset:18432
	ds_read_b128 v[212:215], v10 offset:18496
	ds_read_b128 v[216:219], v10 offset:20736
	ds_read_b128 v[220:223], v10 offset:20800
	ds_read_b128 v[224:227], v10 offset:23040
	ds_read_b128 v[228:231], v10 offset:23104
	v_add_f32_e32 v232, v232, v233
	s_nop 0
	ds_bpermute_b32 v233, v15, v232
	s_waitcnt lgkmcnt(9)
	v_mfma_f32_16x16x32_bf16 v[108:111], v[160:163], v[92:95], 0
	v_mfma_f32_16x16x32_bf16 v[112:115], v[168:171], v[92:95], 0
	v_mfma_f32_16x16x32_bf16 v[116:119], v[176:179], v[92:95], 0
	v_mfma_f32_16x16x32_bf16 v[120:123], v[184:187], v[92:95], 0
	v_mfma_f32_16x16x32_bf16 v[124:127], v[192:195], v[92:95], 0
	v_mfma_f32_16x16x32_bf16 v[108:111], v[164:167], v[96:99], v[108:111]
	v_mfma_f32_16x16x32_bf16 v[112:115], v[172:175], v[96:99], v[112:115]
	v_mfma_f32_16x16x32_bf16 v[116:119], v[180:183], v[96:99], v[116:119]
	v_mfma_f32_16x16x32_bf16 v[120:123], v[188:191], v[96:99], v[120:123]
	v_mfma_f32_16x16x32_bf16 v[124:127], v[196:199], v[96:99], v[124:127]
	s_waitcnt lgkmcnt(0)
	v_add_f32_e32 v232, v232, v233
	v_mfma_f32_16x16x32_bf16 v[128:131], v[200:203], v[92:95], 0
	v_mfma_f32_16x16x32_bf16 v[132:135], v[208:211], v[92:95], 0
	v_mfma_f32_16x16x32_bf16 v[136:139], v[216:219], v[92:95], 0
	v_mfma_f32_16x16x32_bf16 v[140:143], v[224:227], v[92:95], 0
	ds_bpermute_b32 v233, v16, v232
	v_mfma_f32_16x16x32_bf16 v[128:131], v[204:207], v[96:99], v[128:131]
	v_mfma_f32_16x16x32_bf16 v[132:135], v[212:215], v[96:99], v[132:135]
	v_mfma_f32_16x16x32_bf16 v[136:139], v[220:223], v[96:99], v[136:139]
	v_mfma_f32_16x16x32_bf16 v[140:143], v[228:231], v[96:99], v[140:143]
	ds_read2_b64 v[160:163], v11 offset0:8 offset1:12
	ds_read2_b64 v[164:167], v12 offset0:8 offset1:12
	ds_read2_b64 v[168:171], v13 offset0:8 offset1:12
	ds_read2_b64 v[172:175], v14 offset0:8 offset1:12
	ds_read2_b64 v[176:179], v11 offset0:16 offset1:20
	ds_read2_b64 v[180:183], v12 offset0:16 offset1:20
	ds_read2_b64 v[184:187], v13 offset0:16 offset1:20
	ds_read2_b64 v[188:191], v14 offset0:16 offset1:20
	ds_read2_b64 v[192:195], v11 offset0:24 offset1:28
	ds_read2_b64 v[196:199], v12 offset0:24 offset1:28
	ds_read2_b64 v[200:203], v13 offset0:24 offset1:28
	ds_read2_b64 v[204:207], v14 offset0:24 offset1:28
	s_waitcnt lgkmcnt(12)
	v_add_f32_e32 v232, v232, v233
	v_mul_f32_e32 v232, 0x3c800000, v232
	v_add_f32_e32 v232, 0x358637bd, v232
	v_rsq_f32_e32 v236, v232
	s_nop 0
	v_mov_b32_e32 v237, v236
	s_nop 1
	v_pk_fma_f32 v[108:109], v[108:109], v[236:237], v[52:53]
	v_pk_fma_f32 v[110:111], v[110:111], v[236:237], v[54:55]
	v_pk_fma_f32 v[112:113], v[112:113], v[236:237], v[56:57]
	v_pk_fma_f32 v[114:115], v[114:115], v[236:237], v[58:59]
	v_pk_fma_f32 v[116:117], v[116:117], v[236:237], v[60:61]
	v_pk_fma_f32 v[118:119], v[118:119], v[236:237], v[62:63]
	v_pk_fma_f32 v[120:121], v[120:121], v[236:237], v[64:65]
	v_pk_fma_f32 v[122:123], v[122:123], v[236:237], v[66:67]
	v_pk_fma_f32 v[124:125], v[124:125], v[236:237], v[68:69]
	v_pk_fma_f32 v[126:127], v[126:127], v[236:237], v[70:71]
	v_pk_fma_f32 v[128:129], v[128:129], v[236:237], v[72:73]
	v_pk_fma_f32 v[130:131], v[130:131], v[236:237], v[74:75]
	v_pk_fma_f32 v[132:133], v[132:133], v[236:237], v[76:77]
	v_pk_fma_f32 v[134:135], v[134:135], v[236:237], v[78:79]
	v_pk_fma_f32 v[136:137], v[136:137], v[236:237], v[80:81]
	v_pk_fma_f32 v[138:139], v[138:139], v[236:237], v[82:83]
	v_pk_fma_f32 v[140:141], v[140:141], v[236:237], v[84:85]
	v_pk_fma_f32 v[142:143], v[142:143], v[236:237], v[86:87]
	v_exp_f32_e32 v108, v108
	v_exp_f32_e32 v109, v109
	v_exp_f32_e32 v110, v110
	v_exp_f32_e32 v111, v111
	v_exp_f32_e32 v112, v112
	v_exp_f32_e32 v113, v113
	v_exp_f32_e32 v114, v114
	v_exp_f32_e32 v115, v115
	v_exp_f32_e32 v116, v116
	v_exp_f32_e32 v117, v117
	v_exp_f32_e32 v118, v118
	v_exp_f32_e32 v119, v119
	v_exp_f32_e32 v120, v120
	v_exp_f32_e32 v121, v121
	v_exp_f32_e32 v122, v122
	v_exp_f32_e32 v123, v123
	v_exp_f32_e32 v124, v124
	v_exp_f32_e32 v125, v125
	v_exp_f32_e32 v126, v126
	v_exp_f32_e32 v127, v127
	v_exp_f32_e32 v128, v128
	v_exp_f32_e32 v129, v129
	v_exp_f32_e32 v130, v130
	v_exp_f32_e32 v131, v131
	v_exp_f32_e32 v132, v132
	v_exp_f32_e32 v133, v133
	v_exp_f32_e32 v134, v134
	v_exp_f32_e32 v135, v135
	v_exp_f32_e32 v136, v136
	v_exp_f32_e32 v137, v137
	v_exp_f32_e32 v138, v138
	v_exp_f32_e32 v139, v139
	v_exp_f32_e32 v140, v140
	v_exp_f32_e32 v141, v141
	v_exp_f32_e32 v142, v142
	v_exp_f32_e32 v143, v143
	s_cmp_lg_u32 s36, 0
	s_cbranch_scc1 .Lat_m2
	v_mov_b32_e32 v108, 0
	v_mov_b32_e32 v109, 0
	v_mov_b32_e32 v110, 0
	v_mov_b32_e32 v111, 0
	v_mov_b32_e32 v112, 0
	v_mov_b32_e32 v113, 0
	v_mov_b32_e32 v114, 0
	v_mov_b32_e32 v115, 0
	v_mov_b32_e32 v116, 0
	v_mov_b32_e32 v117, 0
	v_mov_b32_e32 v118, 0
	v_mov_b32_e32 v119, 0
	v_mov_b32_e32 v120, 0
	v_mov_b32_e32 v121, 0
	v_mov_b32_e32 v122, 0
	v_mov_b32_e32 v123, 0
	v_mov_b32_e32 v124, 0
	v_mov_b32_e32 v125, 0
	v_mov_b32_e32 v126, 0
	v_mov_b32_e32 v127, 0
	v_mov_b32_e32 v128, 0
	v_mov_b32_e32 v129, 0
	v_mov_b32_e32 v130, 0
	v_mov_b32_e32 v131, 0
.Lat_m2:
	s_nop 0
	v_pk_add_f32 v[232:233], v[108:109], v[110:111]
	v_pk_add_f32 v[234:235], v[112:113], v[114:115]
	v_pk_add_f32 v[232:233], v[232:233], v[116:117]
	v_pk_add_f32 v[234:235], v[234:235], v[118:119]
	v_pk_add_f32 v[232:233], v[232:233], v[120:121]
	v_pk_add_f32 v[234:235], v[234:235], v[122:123]
	v_pk_add_f32 v[232:233], v[232:233], v[124:125]
	v_pk_add_f32 v[234:235], v[234:235], v[126:127]
	v_pk_add_f32 v[232:233], v[232:233], v[128:129]
	v_pk_add_f32 v[234:235], v[234:235], v[130:131]
	v_pk_add_f32 v[232:233], v[232:233], v[132:133]
	v_pk_add_f32 v[234:235], v[234:235], v[134:135]
	v_pk_add_f32 v[232:233], v[232:233], v[136:137]
	v_pk_add_f32 v[234:235], v[234:235], v[138:139]
	v_pk_add_f32 v[232:233], v[232:233], v[140:141]
	v_pk_add_f32 v[234:235], v[234:235], v[142:143]
	v_pk_add_f32 v[232:233], v[232:233], v[234:235]
	s_nop 0
	v_add_f32_e32 v232, v232, v233
	v_cvt_pk_bf16_f32 v108, v108, v109
	v_cvt_pk_bf16_f32 v109, v110, v111
	v_cvt_pk_bf16_f32 v110, v112, v113
	v_cvt_pk_bf16_f32 v111, v114, v115
	v_cvt_pk_bf16_f32 v116, v116, v117
	v_cvt_pk_bf16_f32 v117, v118, v119
	v_cvt_pk_bf16_f32 v118, v120, v121
	v_cvt_pk_bf16_f32 v119, v122, v123
	v_cvt_pk_bf16_f32 v124, v124, v125
	v_cvt_pk_bf16_f32 v125, v126, v127
	v_cvt_pk_bf16_f32 v126, v128, v129
	v_cvt_pk_bf16_f32 v127, v130, v131
	v_cvt_pk_bf16_f32 v132, v132, v133
	v_cvt_pk_bf16_f32 v133, v134, v135
	v_cvt_pk_bf16_f32 v134, v136, v137
	v_cvt_pk_bf16_f32 v135, v138, v139
	v_cvt_pk_bf16_f32 v140, v140, v141
	v_cvt_pk_bf16_f32 v141, v142, v143
	v_mov_b32_e32 v142, 0
	v_mov_b32_e32 v143, 0
	ds_bpermute_b32 v233, v15, v232
	s_waitcnt lgkmcnt(1)
	v_mfma_f32_16x16x32_bf16 v[144:147], v[160:163], v[108:111], 0
	v_mfma_f32_16x16x32_bf16 v[148:151], v[164:167], v[108:111], 0
	v_mfma_f32_16x16x32_bf16 v[152:155], v[168:171], v[108:111], 0
	v_mfma_f32_16x16x32_bf16 v[156:159], v[172:175], v[108:111], 0
	v_mfma_f32_16x16x32_bf16 v[144:147], v[176:179], v[116:119], v[144:147]
	v_mfma_f32_16x16x32_bf16 v[148:151], v[180:183], v[116:119], v[148:151]
	v_mfma_f32_16x16x32_bf16 v[152:155], v[184:187], v[116:119], v[152:155]
	v_mfma_f32_16x16x32_bf16 v[156:159], v[188:191], v[116:119], v[156:159]
	v_mfma_f32_16x16x32_bf16 v[144:147], v[192:195], v[124:127], v[144:147]
	v_mfma_f32_16x16x32_bf16 v[148:151], v[196:199], v[124:127], v[148:151]
	v_mfma_f32_16x16x32_bf16 v[152:155], v[200:203], v[124:127], v[152:155]
	v_mfma_f32_16x16x32_bf16 v[156:159], v[204:207], v[124:127], v[156:159]
	ds_read2_b64 v[160:163], v11 offset0:32 offset1:36
	ds_read2_b64 v[164:167], v12 offset0:32 offset1:36
	ds_read2_b64 v[168:171], v13 offset0:32 offset1:36
	ds_read2_b64 v[172:175], v14 offset0:32 offset1:36
	ds_read2_b64 v[176:179], v11 offset0:40 offset1:40
	ds_read2_b64 v[180:183], v12 offset0:40 offset1:40
	ds_read2_b64 v[184:187], v13 offset0:40 offset1:40
	ds_read2_b64 v[188:191], v14 offset0:40 offset1:40
	s_waitcnt lgkmcnt(8)
	v_add_f32_e32 v232, v232, v233
	s_nop 0
	ds_bpermute_b32 v233, v16, v232
	s_waitcnt lgkmcnt(1)
	v_mfma_f32_16x16x32_bf16 v[144:147], v[160:163], v[132:135], v[144:147]
	v_mfma_f32_16x16x32_bf16 v[148:151], v[164:167], v[132:135], v[148:151]
	v_mfma_f32_16x16x32_bf16 v[152:155], v[168:171], v[132:135], v[152:155]
	v_mfma_f32_16x16x32_bf16 v[156:159], v[172:175], v[132:135], v[156:159]
	v_mfma_f32_16x16x32_bf16 v[144:147], v[176:179], v[140:143], v[144:147]
	v_mfma_f32_16x16x32_bf16 v[148:151], v[180:183], v[140:143], v[148:151]
	v_mfma_f32_16x16x32_bf16 v[152:155], v[184:187], v[140:143], v[152:155]
	v_mfma_f32_16x16x32_bf16 v[156:159], v[188:191], v[140:143], v[156:159]
	s_waitcnt lgkmcnt(0)
	v_add_f32_e32 v232, v232, v233
	v_add_f32_e32 v232, v232, v88
	v_rcp_f32_e32 v236, v232
	s_nop 0
	v_mov_b32_e32 v237, v236
	s_nop 4
	v_pk_mul_f32 v[144:145], v[144:145], v[236:237]
	v_pk_mul_f32 v[146:147], v[146:147], v[236:237]
	v_pk_mul_f32 v[148:149], v[148:149], v[236:237]
	v_pk_mul_f32 v[150:151], v[150:151], v[236:237]
	v_pk_mul_f32 v[152:153], v[152:153], v[236:237]
	v_pk_mul_f32 v[154:155], v[154:155], v[236:237]
	v_pk_mul_f32 v[156:157], v[156:157], v[236:237]
	v_pk_mul_f32 v[158:159], v[158:159], v[236:237]
	v_cvt_pk_bf16_f32 v144, v144, v145
	v_cvt_pk_bf16_f32 v145, v146, v147
	v_cvt_pk_bf16_f32 v148, v148, v149
	v_cvt_pk_bf16_f32 v149, v150, v151
	v_cvt_pk_bf16_f32 v152, v152, v153
	v_cvt_pk_bf16_f32 v153, v154, v155
	v_cvt_pk_bf16_f32 v156, v156, v157
	v_cvt_pk_bf16_f32 v157, v158, v159
	global_store_dwordx2 v9, v[144:145], s[50:51] offset:0
	global_store_dwordx2 v9, v[148:149], s[50:51] offset:32
	global_store_dwordx2 v9, v[152:153], s[50:51] offset:64
	global_store_dwordx2 v9, v[156:157], s[50:51] offset:96
	s_add_u32 s50, s50, 0x10000
	s_addc_u32 s51, s51, 0
	s_add_u32 s48, s48, 0x14000
	s_addc_u32 s49, s49, 0
	ds_read_b128 v[160:163], v10 offset:6912
	ds_read_b128 v[164:167], v10 offset:6976
	ds_read_b128 v[168:171], v10 offset:9216
	ds_read_b128 v[172:175], v10 offset:9280
	ds_read_b128 v[176:179], v10 offset:11520
	ds_read_b128 v[180:183], v10 offset:11584
	ds_read_b128 v[184:187], v10 offset:13824
	ds_read_b128 v[188:191], v10 offset:13888
	ds_read_b128 v[192:195], v10 offset:16128
	ds_read_b128 v[196:199], v10 offset:16192
	s_waitcnt vmcnt(4)
	global_load_dwordx4 v[92:95], v8, s[48:49]
	global_load_dwordx4 v[96:99], v8, s[48:49] offset:64
	v_lshlrev_b32_e32 v234, 16, v100
	v_and_b32_e32 v235, 0xffff0000, v100
	v_pk_mul_f32 v[232:233], v[234:235], v[234:235]
	v_lshlrev_b32_e32 v234, 16, v101
	v_and_b32_e32 v235, 0xffff0000, v101
	v_pk_fma_f32 v[232:233], v[234:235], v[234:235], v[232:233]
	v_lshlrev_b32_e32 v234, 16, v102
	v_and_b32_e32 v235, 0xffff0000, v102
	v_pk_fma_f32 v[232:233], v[234:235], v[234:235], v[232:233]
	v_lshlrev_b32_e32 v234, 16, v103
	v_and_b32_e32 v235, 0xffff0000, v103
	v_pk_fma_f32 v[232:233], v[234:235], v[234:235], v[232:233]
	v_lshlrev_b32_e32 v234, 16, v104
	v_and_b32_e32 v235, 0xffff0000, v104
	v_pk_fma_f32 v[232:233], v[234:235], v[234:235], v[232:233]
	v_lshlrev_b32_e32 v234, 16, v105
	v_and_b32_e32 v235, 0xffff0000, v105
	v_pk_fma_f32 v[232:233], v[234:235], v[234:235], v[232:233]
	v_lshlrev_b32_e32 v234, 16, v106
	v_and_b32_e32 v235, 0xffff0000, v106
	v_pk_fma_f32 v[232:233], v[234:235], v[234:235], v[232:233]
	v_lshlrev_b32_e32 v234, 16, v107
	v_and_b32_e32 v235, 0xffff0000, v107
	v_pk_fma_f32 v[232:233], v[234:235], v[234:235], v[232:233]
	ds_read_b128 v[200:203], v10 offset:18432
	ds_read_b128 v[204:207], v10 offset:18496
	ds_read_b128 v[208:211], v10 offset:20736
	ds_read_b128 v[212:215], v10 offset:20800
	ds_read_b128 v[216:219], v10 offset:23040
	ds_read_b128 v[220:223], v10 offset:23104
	ds_read_b128 v[224:227], v10 offset:25344
	ds_read_b128 v[228:231], v10 offset:25408
	v_add_f32_e32 v232, v232, v233
	s_nop 0
	ds_bpermute_b32 v233, v15, v232
	s_waitcnt lgkmcnt(9)
	v_mfma_f32_16x16x32_bf16 v[108:111], v[160:163], v[100:103], 0
	v_mfma_f32_16x16x32_bf16 v[112:115], v[168:171], v[100:103], 0
	v_mfma_f32_16x16x32_bf16 v[116:119], v[176:179], v[100:103], 0
	v_mfma_f32_16x16x32_bf16 v[120:123], v[184:187], v[100:103], 0
	v_mfma_f32_16x16x32_bf16 v[124:127], v[192:195], v[100:103], 0
	v_mfma_f32_16x16x32_bf16 v[108:111], v[164:167], v[104:107], v[108:111]
	v_mfma_f32_16x16x32_bf16 v[112:115], v[172:175], v[104:107], v[112:115]
	v_mfma_f32_16x16x32_bf16 v[116:119], v[180:183], v[104:107], v[116:119]
	v_mfma_f32_16x16x32_bf16 v[120:123], v[188:191], v[104:107], v[120:123]
	v_mfma_f32_16x16x32_bf16 v[124:127], v[196:199], v[104:107], v[124:127]
	s_waitcnt lgkmcnt(0)
	v_add_f32_e32 v232, v232, v233
	v_mfma_f32_16x16x32_bf16 v[128:131], v[200:203], v[100:103], 0
	v_mfma_f32_16x16x32_bf16 v[132:135], v[208:211], v[100:103], 0
	v_mfma_f32_16x16x32_bf16 v[136:139], v[216:219], v[100:103], 0
	v_mfma_f32_16x16x32_bf16 v[140:143], v[224:227], v[100:103], 0
	ds_bpermute_b32 v233, v16, v232
	v_mfma_f32_16x16x32_bf16 v[128:131], v[204:207], v[104:107], v[128:131]
	v_mfma_f32_16x16x32_bf16 v[132:135], v[212:215], v[104:107], v[132:135]
	v_mfma_f32_16x16x32_bf16 v[136:139], v[220:223], v[104:107], v[136:139]
	v_mfma_f32_16x16x32_bf16 v[140:143], v[228:231], v[104:107], v[140:143]
	ds_read2_b64 v[160:163], v11 offset0:12 offset1:16
	ds_read2_b64 v[164:167], v12 offset0:12 offset1:16
	ds_read2_b64 v[168:171], v13 offset0:12 offset1:16
	ds_read2_b64 v[172:175], v14 offset0:12 offset1:16
	ds_read2_b64 v[176:179], v11 offset0:20 offset1:24
	ds_read2_b64 v[180:183], v12 offset0:20 offset1:24
	ds_read2_b64 v[184:187], v13 offset0:20 offset1:24
	ds_read2_b64 v[188:191], v14 offset0:20 offset1:24
	ds_read2_b64 v[192:195], v11 offset0:28 offset1:32
	ds_read2_b64 v[196:199], v12 offset0:28 offset1:32
	ds_read2_b64 v[200:203], v13 offset0:28 offset1:32
	ds_read2_b64 v[204:207], v14 offset0:28 offset1:32
	s_waitcnt lgkmcnt(12)
	v_add_f32_e32 v232, v232, v233
	v_mul_f32_e32 v232, 0x3c800000, v232
	v_add_f32_e32 v232, 0x358637bd, v232
	v_rsq_f32_e32 v236, v232
	s_nop 0
	v_mov_b32_e32 v237, v236
	s_nop 1
	v_pk_fma_f32 v[108:109], v[108:109], v[236:237], v[52:53]
	v_pk_fma_f32 v[110:111], v[110:111], v[236:237], v[54:55]
	v_pk_fma_f32 v[112:113], v[112:113], v[236:237], v[56:57]
	v_pk_fma_f32 v[114:115], v[114:115], v[236:237], v[58:59]
	v_pk_fma_f32 v[116:117], v[116:117], v[236:237], v[60:61]
	v_pk_fma_f32 v[118:119], v[118:119], v[236:237], v[62:63]
	v_pk_fma_f32 v[120:121], v[120:121], v[236:237], v[64:65]
	v_pk_fma_f32 v[122:123], v[122:123], v[236:237], v[66:67]
	v_pk_fma_f32 v[124:125], v[124:125], v[236:237], v[68:69]
	v_pk_fma_f32 v[126:127], v[126:127], v[236:237], v[70:71]
	v_pk_fma_f32 v[128:129], v[128:129], v[236:237], v[72:73]
	v_pk_fma_f32 v[130:131], v[130:131], v[236:237], v[74:75]
	v_pk_fma_f32 v[132:133], v[132:133], v[236:237], v[76:77]
	v_pk_fma_f32 v[134:135], v[134:135], v[236:237], v[78:79]
	v_pk_fma_f32 v[136:137], v[136:137], v[236:237], v[80:81]
	v_pk_fma_f32 v[138:139], v[138:139], v[236:237], v[82:83]
	v_pk_fma_f32 v[140:141], v[140:141], v[236:237], v[84:85]
	v_pk_fma_f32 v[142:143], v[142:143], v[236:237], v[86:87]
	v_exp_f32_e32 v108, v108
	v_exp_f32_e32 v109, v109
	v_exp_f32_e32 v110, v110
	v_exp_f32_e32 v111, v111
	v_exp_f32_e32 v112, v112
	v_exp_f32_e32 v113, v113
	v_exp_f32_e32 v114, v114
	v_exp_f32_e32 v115, v115
	v_exp_f32_e32 v116, v116
	v_exp_f32_e32 v117, v117
	v_exp_f32_e32 v118, v118
	v_exp_f32_e32 v119, v119
	v_exp_f32_e32 v120, v120
	v_exp_f32_e32 v121, v121
	v_exp_f32_e32 v122, v122
	v_exp_f32_e32 v123, v123
	v_exp_f32_e32 v124, v124
	v_exp_f32_e32 v125, v125
	v_exp_f32_e32 v126, v126
	v_exp_f32_e32 v127, v127
	v_exp_f32_e32 v128, v128
	v_exp_f32_e32 v129, v129
	v_exp_f32_e32 v130, v130
	v_exp_f32_e32 v131, v131
	v_exp_f32_e32 v132, v132
	v_exp_f32_e32 v133, v133
	v_exp_f32_e32 v134, v134
	v_exp_f32_e32 v135, v135
	v_exp_f32_e32 v136, v136
	v_exp_f32_e32 v137, v137
	v_exp_f32_e32 v138, v138
	v_exp_f32_e32 v139, v139
	v_exp_f32_e32 v140, v140
	v_exp_f32_e32 v141, v141
	v_exp_f32_e32 v142, v142
	v_exp_f32_e32 v143, v143
	s_cmp_lg_u32 s36, 0
	s_cbranch_scc1 .Lat_m3
	v_mov_b32_e32 v108, 0
	v_mov_b32_e32 v109, 0
	v_mov_b32_e32 v110, 0
	v_mov_b32_e32 v111, 0
	v_mov_b32_e32 v112, 0
	v_mov_b32_e32 v113, 0
	v_mov_b32_e32 v114, 0
	v_mov_b32_e32 v115, 0
	v_mov_b32_e32 v116, 0
	v_mov_b32_e32 v117, 0
	v_mov_b32_e32 v118, 0
	v_mov_b32_e32 v119, 0
	v_mov_b32_e32 v120, 0
	v_mov_b32_e32 v121, 0
	v_mov_b32_e32 v122, 0
	v_mov_b32_e32 v123, 0
	v_mov_b32_e32 v124, 0
	v_mov_b32_e32 v125, 0
	v_mov_b32_e32 v126, 0
	v_mov_b32_e32 v127, 0
.Lat_m3:
	s_nop 0
	v_pk_add_f32 v[232:233], v[108:109], v[110:111]
	v_pk_add_f32 v[234:235], v[112:113], v[114:115]
	v_pk_add_f32 v[232:233], v[232:233], v[116:117]
	v_pk_add_f32 v[234:235], v[234:235], v[118:119]
	v_pk_add_f32 v[232:233], v[232:233], v[120:121]
	v_pk_add_f32 v[234:235], v[234:235], v[122:123]
	v_pk_add_f32 v[232:233], v[232:233], v[124:125]
	v_pk_add_f32 v[234:235], v[234:235], v[126:127]
	v_pk_add_f32 v[232:233], v[232:233], v[128:129]
	v_pk_add_f32 v[234:235], v[234:235], v[130:131]
	v_pk_add_f32 v[232:233], v[232:233], v[132:133]
	v_pk_add_f32 v[234:235], v[234:235], v[134:135]
	v_pk_add_f32 v[232:233], v[232:233], v[136:137]
	v_pk_add_f32 v[234:235], v[234:235], v[138:139]
	v_pk_add_f32 v[232:233], v[232:233], v[140:141]
	v_pk_add_f32 v[234:235], v[234:235], v[142:143]
	v_pk_add_f32 v[232:233], v[232:233], v[234:235]
	s_nop 0
	v_add_f32_e32 v232, v232, v233
	v_cvt_pk_bf16_f32 v108, v108, v109
	v_cvt_pk_bf16_f32 v109, v110, v111
	v_cvt_pk_bf16_f32 v110, v112, v113
	v_cvt_pk_bf16_f32 v111, v114, v115
	v_cvt_pk_bf16_f32 v116, v116, v117
	v_cvt_pk_bf16_f32 v117, v118, v119
	v_cvt_pk_bf16_f32 v118, v120, v121
	v_cvt_pk_bf16_f32 v119, v122, v123
	v_cvt_pk_bf16_f32 v124, v124, v125
	v_cvt_pk_bf16_f32 v125, v126, v127
	v_cvt_pk_bf16_f32 v126, v128, v129
	v_cvt_pk_bf16_f32 v127, v130, v131
	v_cvt_pk_bf16_f32 v132, v132, v133
	v_cvt_pk_bf16_f32 v133, v134, v135
	v_cvt_pk_bf16_f32 v134, v136, v137
	v_cvt_pk_bf16_f32 v135, v138, v139
	v_cvt_pk_bf16_f32 v140, v140, v141
	v_cvt_pk_bf16_f32 v141, v142, v143
	v_mov_b32_e32 v142, 0
	v_mov_b32_e32 v143, 0
	ds_bpermute_b32 v233, v15, v232
	s_waitcnt lgkmcnt(1)
	v_mfma_f32_16x16x32_bf16 v[144:147], v[160:163], v[108:111], 0
	v_mfma_f32_16x16x32_bf16 v[148:151], v[164:167], v[108:111], 0
	v_mfma_f32_16x16x32_bf16 v[152:155], v[168:171], v[108:111], 0
	v_mfma_f32_16x16x32_bf16 v[156:159], v[172:175], v[108:111], 0
	v_mfma_f32_16x16x32_bf16 v[144:147], v[176:179], v[116:119], v[144:147]
	v_mfma_f32_16x16x32_bf16 v[148:151], v[180:183], v[116:119], v[148:151]
	v_mfma_f32_16x16x32_bf16 v[152:155], v[184:187], v[116:119], v[152:155]
	v_mfma_f32_16x16x32_bf16 v[156:159], v[188:191], v[116:119], v[156:159]
	v_mfma_f32_16x16x32_bf16 v[144:147], v[192:195], v[124:127], v[144:147]
	v_mfma_f32_16x16x32_bf16 v[148:151], v[196:199], v[124:127], v[148:151]
	v_mfma_f32_16x16x32_bf16 v[152:155], v[200:203], v[124:127], v[152:155]
	v_mfma_f32_16x16x32_bf16 v[156:159], v[204:207], v[124:127], v[156:159]
	ds_read2_b64 v[160:163], v11 offset0:36 offset1:40
	ds_read2_b64 v[164:167], v12 offset0:36 offset1:40
	ds_read2_b64 v[168:171], v13 offset0:36 offset1:40
	ds_read2_b64 v[172:175], v14 offset0:36 offset1:40
	ds_read2_b64 v[176:179], v11 offset0:44 offset1:44
	ds_read2_b64 v[180:183], v12 offset0:44 offset1:44
	ds_read2_b64 v[184:187], v13 offset0:44 offset1:44
	ds_read2_b64 v[188:191], v14 offset0:44 offset1:44
	s_waitcnt lgkmcnt(8)
	v_add_f32_e32 v232, v232, v233
	s_nop 0
	ds_bpermute_b32 v233, v16, v232
	s_waitcnt lgkmcnt(1)
	v_mfma_f32_16x16x32_bf16 v[144:147], v[160:163], v[132:135], v[144:147]
	v_mfma_f32_16x16x32_bf16 v[148:151], v[164:167], v[132:135], v[148:151]
	v_mfma_f32_16x16x32_bf16 v[152:155], v[168:171], v[132:135], v[152:155]
	v_mfma_f32_16x16x32_bf16 v[156:159], v[172:175], v[132:135], v[156:159]
	v_mfma_f32_16x16x32_bf16 v[144:147], v[176:179], v[140:143], v[144:147]
	v_mfma_f32_16x16x32_bf16 v[148:151], v[180:183], v[140:143], v[148:151]
	v_mfma_f32_16x16x32_bf16 v[152:155], v[184:187], v[140:143], v[152:155]
	v_mfma_f32_16x16x32_bf16 v[156:159], v[188:191], v[140:143], v[156:159]
	s_waitcnt lgkmcnt(0)
	v_add_f32_e32 v232, v232, v233
	v_add_f32_e32 v232, v232, v88
	v_rcp_f32_e32 v236, v232
	s_nop 0
	v_mov_b32_e32 v237, v236
	s_nop 4
	v_pk_mul_f32 v[144:145], v[144:145], v[236:237]
	v_pk_mul_f32 v[146:147], v[146:147], v[236:237]
	v_pk_mul_f32 v[148:149], v[148:149], v[236:237]
	v_pk_mul_f32 v[150:151], v[150:151], v[236:237]
	v_pk_mul_f32 v[152:153], v[152:153], v[236:237]
	v_pk_mul_f32 v[154:155], v[154:155], v[236:237]
	v_pk_mul_f32 v[156:157], v[156:157], v[236:237]
	v_pk_mul_f32 v[158:159], v[158:159], v[236:237]
	v_cvt_pk_bf16_f32 v144, v144, v145
	v_cvt_pk_bf16_f32 v145, v146, v147
	v_cvt_pk_bf16_f32 v148, v148, v149
	v_cvt_pk_bf16_f32 v149, v150, v151
	v_cvt_pk_bf16_f32 v152, v152, v153
	v_cvt_pk_bf16_f32 v153, v154, v155
	v_cvt_pk_bf16_f32 v156, v156, v157
	v_cvt_pk_bf16_f32 v157, v158, v159
	global_store_dwordx2 v9, v[144:145], s[50:51] offset:0
	global_store_dwordx2 v9, v[148:149], s[50:51] offset:32
	global_store_dwordx2 v9, v[152:153], s[50:51] offset:64
	global_store_dwordx2 v9, v[156:157], s[50:51] offset:96
	s_add_u32 s50, s50, 0x10000
	s_addc_u32 s51, s51, 0
	s_add_u32 s48, s48, 0x14000
	s_addc_u32 s49, s49, 0
	ds_read_b128 v[160:163], v10 offset:9216
	ds_read_b128 v[164:167], v10 offset:9280
	ds_read_b128 v[168:171], v10 offset:11520
	ds_read_b128 v[172:175], v10 offset:11584
	ds_read_b128 v[176:179], v10 offset:13824
	ds_read_b128 v[180:183], v10 offset:13888
	ds_read_b128 v[184:187], v10 offset:16128
	ds_read_b128 v[188:191], v10 offset:16192
	ds_read_b128 v[192:195], v10 offset:18432
	ds_read_b128 v[196:199], v10 offset:18496
	s_waitcnt vmcnt(4)
	global_load_dwordx4 v[100:103], v8, s[48:49]
	global_load_dwordx4 v[104:107], v8, s[48:49] offset:64
	v_lshlrev_b32_e32 v234, 16, v92
	v_and_b32_e32 v235, 0xffff0000, v92
	v_pk_mul_f32 v[232:233], v[234:235], v[234:235]
	v_lshlrev_b32_e32 v234, 16, v93
	v_and_b32_e32 v235, 0xffff0000, v93
	v_pk_fma_f32 v[232:233], v[234:235], v[234:235], v[232:233]
	v_lshlrev_b32_e32 v234, 16, v94
	v_and_b32_e32 v235, 0xffff0000, v94
	v_pk_fma_f32 v[232:233], v[234:235], v[234:235], v[232:233]
	v_lshlrev_b32_e32 v234, 16, v95
	v_and_b32_e32 v235, 0xffff0000, v95
	v_pk_fma_f32 v[232:233], v[234:235], v[234:235], v[232:233]
	v_lshlrev_b32_e32 v234, 16, v96
	v_and_b32_e32 v235, 0xffff0000, v96
	v_pk_fma_f32 v[232:233], v[234:235], v[234:235], v[232:233]
	v_lshlrev_b32_e32 v234, 16, v97
	v_and_b32_e32 v235, 0xffff0000, v97
	v_pk_fma_f32 v[232:233], v[234:235], v[234:235], v[232:233]
	v_lshlrev_b32_e32 v234, 16, v98
	v_and_b32_e32 v235, 0xffff0000, v98
	v_pk_fma_f32 v[232:233], v[234:235], v[234:235], v[232:233]
	v_lshlrev_b32_e32 v234, 16, v99
	v_and_b32_e32 v235, 0xffff0000, v99
	v_pk_fma_f32 v[232:233], v[234:235], v[234:235], v[232:233]
	ds_read_b128 v[200:203], v10 offset:20736
	ds_read_b128 v[204:207], v10 offset:20800
	ds_read_b128 v[208:211], v10 offset:23040
	ds_read_b128 v[212:215], v10 offset:23104
	ds_read_b128 v[216:219], v10 offset:25344
	ds_read_b128 v[220:223], v10 offset:25408
	ds_read_b128 v[224:227], v10 offset:27648
	ds_read_b128 v[228:231], v10 offset:27712
	v_add_f32_e32 v232, v232, v233
	s_nop 0
	ds_bpermute_b32 v233, v15, v232
	s_waitcnt lgkmcnt(9)
	v_mfma_f32_16x16x32_bf16 v[108:111], v[160:163], v[92:95], 0
	v_mfma_f32_16x16x32_bf16 v[112:115], v[168:171], v[92:95], 0
	v_mfma_f32_16x16x32_bf16 v[116:119], v[176:179], v[92:95], 0
	v_mfma_f32_16x16x32_bf16 v[120:123], v[184:187], v[92:95], 0
	v_mfma_f32_16x16x32_bf16 v[124:127], v[192:195], v[92:95], 0
	v_mfma_f32_16x16x32_bf16 v[108:111], v[164:167], v[96:99], v[108:111]
	v_mfma_f32_16x16x32_bf16 v[112:115], v[172:175], v[96:99], v[112:115]
	v_mfma_f32_16x16x32_bf16 v[116:119], v[180:183], v[96:99], v[116:119]
	v_mfma_f32_16x16x32_bf16 v[120:123], v[188:191], v[96:99], v[120:123]
	v_mfma_f32_16x16x32_bf16 v[124:127], v[196:199], v[96:99], v[124:127]
	s_waitcnt lgkmcnt(0)
	v_add_f32_e32 v232, v232, v233
	v_mfma_f32_16x16x32_bf16 v[128:131], v[200:203], v[92:95], 0
	v_mfma_f32_16x16x32_bf16 v[132:135], v[208:211], v[92:95], 0
	v_mfma_f32_16x16x32_bf16 v[136:139], v[216:219], v[92:95], 0
	v_mfma_f32_16x16x32_bf16 v[140:143], v[224:227], v[92:95], 0
	ds_bpermute_b32 v233, v16, v232
	v_mfma_f32_16x16x32_bf16 v[128:131], v[204:207], v[96:99], v[128:131]
	v_mfma_f32_16x16x32_bf16 v[132:135], v[212:215], v[96:99], v[132:135]
	v_mfma_f32_16x16x32_bf16 v[136:139], v[220:223], v[96:99], v[136:139]
	v_mfma_f32_16x16x32_bf16 v[140:143], v[228:231], v[96:99], v[140:143]
	ds_read2_b64 v[160:163], v11 offset0:16 offset1:20
	ds_read2_b64 v[164:167], v12 offset0:16 offset1:20
	ds_read2_b64 v[168:171], v13 offset0:16 offset1:20
	ds_read2_b64 v[172:175], v14 offset0:16 offset1:20
	ds_read2_b64 v[176:179], v11 offset0:24 offset1:28
	ds_read2_b64 v[180:183], v12 offset0:24 offset1:28
	ds_read2_b64 v[184:187], v13 offset0:24 offset1:28
	ds_read2_b64 v[188:191], v14 offset0:24 offset1:28
	ds_read2_b64 v[192:195], v11 offset0:32 offset1:36
	ds_read2_b64 v[196:199], v12 offset0:32 offset1:36
	ds_read2_b64 v[200:203], v13 offset0:32 offset1:36
	ds_read2_b64 v[204:207], v14 offset0:32 offset1:36
	s_waitcnt lgkmcnt(12)
	v_add_f32_e32 v232, v232, v233
	v_mul_f32_e32 v232, 0x3c800000, v232
	v_add_f32_e32 v232, 0x358637bd, v232
	v_rsq_f32_e32 v236, v232
	s_nop 0
	v_mov_b32_e32 v237, v236
	s_nop 1
	v_pk_fma_f32 v[108:109], v[108:109], v[236:237], v[52:53]
	v_pk_fma_f32 v[110:111], v[110:111], v[236:237], v[54:55]
	v_pk_fma_f32 v[112:113], v[112:113], v[236:237], v[56:57]
	v_pk_fma_f32 v[114:115], v[114:115], v[236:237], v[58:59]
	v_pk_fma_f32 v[116:117], v[116:117], v[236:237], v[60:61]
	v_pk_fma_f32 v[118:119], v[118:119], v[236:237], v[62:63]
	v_pk_fma_f32 v[120:121], v[120:121], v[236:237], v[64:65]
	v_pk_fma_f32 v[122:123], v[122:123], v[236:237], v[66:67]
	v_pk_fma_f32 v[124:125], v[124:125], v[236:237], v[68:69]
	v_pk_fma_f32 v[126:127], v[126:127], v[236:237], v[70:71]
	v_pk_fma_f32 v[128:129], v[128:129], v[236:237], v[72:73]
	v_pk_fma_f32 v[130:131], v[130:131], v[236:237], v[74:75]
	v_pk_fma_f32 v[132:133], v[132:133], v[236:237], v[76:77]
	v_pk_fma_f32 v[134:135], v[134:135], v[236:237], v[78:79]
	v_pk_fma_f32 v[136:137], v[136:137], v[236:237], v[80:81]
	v_pk_fma_f32 v[138:139], v[138:139], v[236:237], v[82:83]
	v_pk_fma_f32 v[140:141], v[140:141], v[236:237], v[84:85]
	v_pk_fma_f32 v[142:143], v[142:143], v[236:237], v[86:87]
	v_exp_f32_e32 v108, v108
	v_exp_f32_e32 v109, v109
	v_exp_f32_e32 v110, v110
	v_exp_f32_e32 v111, v111
	v_exp_f32_e32 v112, v112
	v_exp_f32_e32 v113, v113
	v_exp_f32_e32 v114, v114
	v_exp_f32_e32 v115, v115
	v_exp_f32_e32 v116, v116
	v_exp_f32_e32 v117, v117
	v_exp_f32_e32 v118, v118
	v_exp_f32_e32 v119, v119
	v_exp_f32_e32 v120, v120
	v_exp_f32_e32 v121, v121
	v_exp_f32_e32 v122, v122
	v_exp_f32_e32 v123, v123
	v_exp_f32_e32 v124, v124
	v_exp_f32_e32 v125, v125
	v_exp_f32_e32 v126, v126
	v_exp_f32_e32 v127, v127
	v_exp_f32_e32 v128, v128
	v_exp_f32_e32 v129, v129
	v_exp_f32_e32 v130, v130
	v_exp_f32_e32 v131, v131
	v_exp_f32_e32 v132, v132
	v_exp_f32_e32 v133, v133
	v_exp_f32_e32 v134, v134
	v_exp_f32_e32 v135, v135
	v_exp_f32_e32 v136, v136
	v_exp_f32_e32 v137, v137
	v_exp_f32_e32 v138, v138
	v_exp_f32_e32 v139, v139
	v_exp_f32_e32 v140, v140
	v_exp_f32_e32 v141, v141
	v_exp_f32_e32 v142, v142
	v_exp_f32_e32 v143, v143
	s_cmp_lg_u32 s36, 0
	s_cbranch_scc1 .Lat_m4
	v_mov_b32_e32 v108, 0
	v_mov_b32_e32 v109, 0
	v_mov_b32_e32 v110, 0
	v_mov_b32_e32 v111, 0
	v_mov_b32_e32 v112, 0
	v_mov_b32_e32 v113, 0
	v_mov_b32_e32 v114, 0
	v_mov_b32_e32 v115, 0
	v_mov_b32_e32 v116, 0
	v_mov_b32_e32 v117, 0
	v_mov_b32_e32 v118, 0
	v_mov_b32_e32 v119, 0
	v_mov_b32_e32 v120, 0
	v_mov_b32_e32 v121, 0
	v_mov_b32_e32 v122, 0
	v_mov_b32_e32 v123, 0
.Lat_m4:
	s_nop 0
	v_pk_add_f32 v[232:233], v[108:109], v[110:111]
	v_pk_add_f32 v[234:235], v[112:113], v[114:115]
	v_pk_add_f32 v[232:233], v[232:233], v[116:117]
	v_pk_add_f32 v[234:235], v[234:235], v[118:119]
	v_pk_add_f32 v[232:233], v[232:233], v[120:121]
	v_pk_add_f32 v[234:235], v[234:235], v[122:123]
	v_pk_add_f32 v[232:233], v[232:233], v[124:125]
	v_pk_add_f32 v[234:235], v[234:235], v[126:127]
	v_pk_add_f32 v[232:233], v[232:233], v[128:129]
	v_pk_add_f32 v[234:235], v[234:235], v[130:131]
	v_pk_add_f32 v[232:233], v[232:233], v[132:133]
	v_pk_add_f32 v[234:235], v[234:235], v[134:135]
	v_pk_add_f32 v[232:233], v[232:233], v[136:137]
	v_pk_add_f32 v[234:235], v[234:235], v[138:139]
	v_pk_add_f32 v[232:233], v[232:233], v[140:141]
	v_pk_add_f32 v[234:235], v[234:235], v[142:143]
	v_pk_add_f32 v[232:233], v[232:233], v[234:235]
	s_nop 0
	v_add_f32_e32 v232, v232, v233
	v_cvt_pk_bf16_f32 v108, v108, v109
	v_cvt_pk_bf16_f32 v109, v110, v111
	v_cvt_pk_bf16_f32 v110, v112, v113
	v_cvt_pk_bf16_f32 v111, v114, v115
	v_cvt_pk_bf16_f32 v116, v116, v117
	v_cvt_pk_bf16_f32 v117, v118, v119
	v_cvt_pk_bf16_f32 v118, v120, v121
	v_cvt_pk_bf16_f32 v119, v122, v123
	v_cvt_pk_bf16_f32 v124, v124, v125
	v_cvt_pk_bf16_f32 v125, v126, v127
	v_cvt_pk_bf16_f32 v126, v128, v129
	v_cvt_pk_bf16_f32 v127, v130, v131
	v_cvt_pk_bf16_f32 v132, v132, v133
	v_cvt_pk_bf16_f32 v133, v134, v135
	v_cvt_pk_bf16_f32 v134, v136, v137
	v_cvt_pk_bf16_f32 v135, v138, v139
	v_cvt_pk_bf16_f32 v140, v140, v141
	v_cvt_pk_bf16_f32 v141, v142, v143
	v_mov_b32_e32 v142, 0
	v_mov_b32_e32 v143, 0
	ds_bpermute_b32 v233, v15, v232
	s_waitcnt lgkmcnt(1)
	v_mfma_f32_16x16x32_bf16 v[144:147], v[160:163], v[108:111], 0
	v_mfma_f32_16x16x32_bf16 v[148:151], v[164:167], v[108:111], 0
	v_mfma_f32_16x16x32_bf16 v[152:155], v[168:171], v[108:111], 0
	v_mfma_f32_16x16x32_bf16 v[156:159], v[172:175], v[108:111], 0
	v_mfma_f32_16x16x32_bf16 v[144:147], v[176:179], v[116:119], v[144:147]
	v_mfma_f32_16x16x32_bf16 v[148:151], v[180:183], v[116:119], v[148:151]
	v_mfma_f32_16x16x32_bf16 v[152:155], v[184:187], v[116:119], v[152:155]
	v_mfma_f32_16x16x32_bf16 v[156:159], v[188:191], v[116:119], v[156:159]
	v_mfma_f32_16x16x32_bf16 v[144:147], v[192:195], v[124:127], v[144:147]
	v_mfma_f32_16x16x32_bf16 v[148:151], v[196:199], v[124:127], v[148:151]
	v_mfma_f32_16x16x32_bf16 v[152:155], v[200:203], v[124:127], v[152:155]
	v_mfma_f32_16x16x32_bf16 v[156:159], v[204:207], v[124:127], v[156:159]
	ds_read2_b64 v[160:163], v11 offset0:40 offset1:44
	ds_read2_b64 v[164:167], v12 offset0:40 offset1:44
	ds_read2_b64 v[168:171], v13 offset0:40 offset1:44
	ds_read2_b64 v[172:175], v14 offset0:40 offset1:44
	ds_read2_b64 v[176:179], v11 offset0:48 offset1:48
	ds_read2_b64 v[180:183], v12 offset0:48 offset1:48
	ds_read2_b64 v[184:187], v13 offset0:48 offset1:48
	ds_read2_b64 v[188:191], v14 offset0:48 offset1:48
	s_waitcnt lgkmcnt(8)
	v_add_f32_e32 v232, v232, v233
	s_nop 0
	ds_bpermute_b32 v233, v16, v232
	s_waitcnt lgkmcnt(1)
	v_mfma_f32_16x16x32_bf16 v[144:147], v[160:163], v[132:135], v[144:147]
	v_mfma_f32_16x16x32_bf16 v[148:151], v[164:167], v[132:135], v[148:151]
	v_mfma_f32_16x16x32_bf16 v[152:155], v[168:171], v[132:135], v[152:155]
	v_mfma_f32_16x16x32_bf16 v[156:159], v[172:175], v[132:135], v[156:159]
	v_mfma_f32_16x16x32_bf16 v[144:147], v[176:179], v[140:143], v[144:147]
	v_mfma_f32_16x16x32_bf16 v[148:151], v[180:183], v[140:143], v[148:151]
	v_mfma_f32_16x16x32_bf16 v[152:155], v[184:187], v[140:143], v[152:155]
	v_mfma_f32_16x16x32_bf16 v[156:159], v[188:191], v[140:143], v[156:159]
	s_waitcnt lgkmcnt(0)
	v_add_f32_e32 v232, v232, v233
	v_add_f32_e32 v232, v232, v88
	v_rcp_f32_e32 v236, v232
	s_nop 0
	v_mov_b32_e32 v237, v236
	s_nop 4
	v_pk_mul_f32 v[144:145], v[144:145], v[236:237]
	v_pk_mul_f32 v[146:147], v[146:147], v[236:237]
	v_pk_mul_f32 v[148:149], v[148:149], v[236:237]
	v_pk_mul_f32 v[150:151], v[150:151], v[236:237]
	v_pk_mul_f32 v[152:153], v[152:153], v[236:237]
	v_pk_mul_f32 v[154:155], v[154:155], v[236:237]
	v_pk_mul_f32 v[156:157], v[156:157], v[236:237]
	v_pk_mul_f32 v[158:159], v[158:159], v[236:237]
	v_cvt_pk_bf16_f32 v144, v144, v145
	v_cvt_pk_bf16_f32 v145, v146, v147
	v_cvt_pk_bf16_f32 v148, v148, v149
	v_cvt_pk_bf16_f32 v149, v150, v151
	v_cvt_pk_bf16_f32 v152, v152, v153
	v_cvt_pk_bf16_f32 v153, v154, v155
	v_cvt_pk_bf16_f32 v156, v156, v157
	v_cvt_pk_bf16_f32 v157, v158, v159
	global_store_dwordx2 v9, v[144:145], s[50:51] offset:0
	global_store_dwordx2 v9, v[148:149], s[50:51] offset:32
	global_store_dwordx2 v9, v[152:153], s[50:51] offset:64
	global_store_dwordx2 v9, v[156:157], s[50:51] offset:96
	s_add_u32 s50, s50, 0x10000
	s_addc_u32 s51, s51, 0
	s_add_u32 s48, s48, 0x14000
	s_addc_u32 s49, s49, 0
	ds_read_b128 v[160:163], v10 offset:11520
	ds_read_b128 v[164:167], v10 offset:11584
	ds_read_b128 v[168:171], v10 offset:13824
	ds_read_b128 v[172:175], v10 offset:13888
	ds_read_b128 v[176:179], v10 offset:16128
	ds_read_b128 v[180:183], v10 offset:16192
	ds_read_b128 v[184:187], v10 offset:18432
	ds_read_b128 v[188:191], v10 offset:18496
	ds_read_b128 v[192:195], v10 offset:20736
	ds_read_b128 v[196:199], v10 offset:20800
	s_waitcnt vmcnt(4)
	global_load_dwordx4 v[92:95], v8, s[48:49]
	global_load_dwordx4 v[96:99], v8, s[48:49] offset:64
	v_lshlrev_b32_e32 v234, 16, v100
	v_and_b32_e32 v235, 0xffff0000, v100
	v_pk_mul_f32 v[232:233], v[234:235], v[234:235]
	v_lshlrev_b32_e32 v234, 16, v101
	v_and_b32_e32 v235, 0xffff0000, v101
	v_pk_fma_f32 v[232:233], v[234:235], v[234:235], v[232:233]
	v_lshlrev_b32_e32 v234, 16, v102
	v_and_b32_e32 v235, 0xffff0000, v102
	v_pk_fma_f32 v[232:233], v[234:235], v[234:235], v[232:233]
	v_lshlrev_b32_e32 v234, 16, v103
	v_and_b32_e32 v235, 0xffff0000, v103
	v_pk_fma_f32 v[232:233], v[234:235], v[234:235], v[232:233]
	v_lshlrev_b32_e32 v234, 16, v104
	v_and_b32_e32 v235, 0xffff0000, v104
	v_pk_fma_f32 v[232:233], v[234:235], v[234:235], v[232:233]
	v_lshlrev_b32_e32 v234, 16, v105
	v_and_b32_e32 v235, 0xffff0000, v105
	v_pk_fma_f32 v[232:233], v[234:235], v[234:235], v[232:233]
	v_lshlrev_b32_e32 v234, 16, v106
	v_and_b32_e32 v235, 0xffff0000, v106
	v_pk_fma_f32 v[232:233], v[234:235], v[234:235], v[232:233]
	v_lshlrev_b32_e32 v234, 16, v107
	v_and_b32_e32 v235, 0xffff0000, v107
	v_pk_fma_f32 v[232:233], v[234:235], v[234:235], v[232:233]
	ds_read_b128 v[200:203], v10 offset:23040
	ds_read_b128 v[204:207], v10 offset:23104
	ds_read_b128 v[208:211], v10 offset:25344
	ds_read_b128 v[212:215], v10 offset:25408
	ds_read_b128 v[216:219], v10 offset:27648
	ds_read_b128 v[220:223], v10 offset:27712
	ds_read_b128 v[224:227], v10 offset:29952
	ds_read_b128 v[228:231], v10 offset:30016
	v_add_f32_e32 v232, v232, v233
	s_nop 0
	ds_bpermute_b32 v233, v15, v232
	s_waitcnt lgkmcnt(9)
	v_mfma_f32_16x16x32_bf16 v[108:111], v[160:163], v[100:103], 0
	v_mfma_f32_16x16x32_bf16 v[112:115], v[168:171], v[100:103], 0
	v_mfma_f32_16x16x32_bf16 v[116:119], v[176:179], v[100:103], 0
	v_mfma_f32_16x16x32_bf16 v[120:123], v[184:187], v[100:103], 0
	v_mfma_f32_16x16x32_bf16 v[124:127], v[192:195], v[100:103], 0
	v_mfma_f32_16x16x32_bf16 v[108:111], v[164:167], v[104:107], v[108:111]
	v_mfma_f32_16x16x32_bf16 v[112:115], v[172:175], v[104:107], v[112:115]
	v_mfma_f32_16x16x32_bf16 v[116:119], v[180:183], v[104:107], v[116:119]
	v_mfma_f32_16x16x32_bf16 v[120:123], v[188:191], v[104:107], v[120:123]
	v_mfma_f32_16x16x32_bf16 v[124:127], v[196:199], v[104:107], v[124:127]
	s_waitcnt lgkmcnt(0)
	v_add_f32_e32 v232, v232, v233
	v_mfma_f32_16x16x32_bf16 v[128:131], v[200:203], v[100:103], 0
	v_mfma_f32_16x16x32_bf16 v[132:135], v[208:211], v[100:103], 0
	v_mfma_f32_16x16x32_bf16 v[136:139], v[216:219], v[100:103], 0
	v_mfma_f32_16x16x32_bf16 v[140:143], v[224:227], v[100:103], 0
	ds_bpermute_b32 v233, v16, v232
	v_mfma_f32_16x16x32_bf16 v[128:131], v[204:207], v[104:107], v[128:131]
	v_mfma_f32_16x16x32_bf16 v[132:135], v[212:215], v[104:107], v[132:135]
	v_mfma_f32_16x16x32_bf16 v[136:139], v[220:223], v[104:107], v[136:139]
	v_mfma_f32_16x16x32_bf16 v[140:143], v[228:231], v[104:107], v[140:143]
	ds_read2_b64 v[160:163], v11 offset0:20 offset1:24
	ds_read2_b64 v[164:167], v12 offset0:20 offset1:24
	ds_read2_b64 v[168:171], v13 offset0:20 offset1:24
	ds_read2_b64 v[172:175], v14 offset0:20 offset1:24
	ds_read2_b64 v[176:179], v11 offset0:28 offset1:32
	ds_read2_b64 v[180:183], v12 offset0:28 offset1:32
	ds_read2_b64 v[184:187], v13 offset0:28 offset1:32
	ds_read2_b64 v[188:191], v14 offset0:28 offset1:32
	ds_read2_b64 v[192:195], v11 offset0:36 offset1:40
	ds_read2_b64 v[196:199], v12 offset0:36 offset1:40
	ds_read2_b64 v[200:203], v13 offset0:36 offset1:40
	ds_read2_b64 v[204:207], v14 offset0:36 offset1:40
	s_waitcnt lgkmcnt(12)
	v_add_f32_e32 v232, v232, v233
	v_mul_f32_e32 v232, 0x3c800000, v232
	v_add_f32_e32 v232, 0x358637bd, v232
	v_rsq_f32_e32 v236, v232
	s_nop 0
	v_mov_b32_e32 v237, v236
	s_nop 1
	v_pk_fma_f32 v[108:109], v[108:109], v[236:237], v[52:53]
	v_pk_fma_f32 v[110:111], v[110:111], v[236:237], v[54:55]
	v_pk_fma_f32 v[112:113], v[112:113], v[236:237], v[56:57]
	v_pk_fma_f32 v[114:115], v[114:115], v[236:237], v[58:59]
	v_pk_fma_f32 v[116:117], v[116:117], v[236:237], v[60:61]
	v_pk_fma_f32 v[118:119], v[118:119], v[236:237], v[62:63]
	v_pk_fma_f32 v[120:121], v[120:121], v[236:237], v[64:65]
	v_pk_fma_f32 v[122:123], v[122:123], v[236:237], v[66:67]
	v_pk_fma_f32 v[124:125], v[124:125], v[236:237], v[68:69]
	v_pk_fma_f32 v[126:127], v[126:127], v[236:237], v[70:71]
	v_pk_fma_f32 v[128:129], v[128:129], v[236:237], v[72:73]
	v_pk_fma_f32 v[130:131], v[130:131], v[236:237], v[74:75]
	v_pk_fma_f32 v[132:133], v[132:133], v[236:237], v[76:77]
	v_pk_fma_f32 v[134:135], v[134:135], v[236:237], v[78:79]
	v_pk_fma_f32 v[136:137], v[136:137], v[236:237], v[80:81]
	v_pk_fma_f32 v[138:139], v[138:139], v[236:237], v[82:83]
	v_pk_fma_f32 v[140:141], v[140:141], v[236:237], v[84:85]
	v_pk_fma_f32 v[142:143], v[142:143], v[236:237], v[86:87]
	v_exp_f32_e32 v108, v108
	v_exp_f32_e32 v109, v109
	v_exp_f32_e32 v110, v110
	v_exp_f32_e32 v111, v111
	v_exp_f32_e32 v112, v112
	v_exp_f32_e32 v113, v113
	v_exp_f32_e32 v114, v114
	v_exp_f32_e32 v115, v115
	v_exp_f32_e32 v116, v116
	v_exp_f32_e32 v117, v117
	v_exp_f32_e32 v118, v118
	v_exp_f32_e32 v119, v119
	v_exp_f32_e32 v120, v120
	v_exp_f32_e32 v121, v121
	v_exp_f32_e32 v122, v122
	v_exp_f32_e32 v123, v123
	v_exp_f32_e32 v124, v124
	v_exp_f32_e32 v125, v125
	v_exp_f32_e32 v126, v126
	v_exp_f32_e32 v127, v127
	v_exp_f32_e32 v128, v128
	v_exp_f32_e32 v129, v129
	v_exp_f32_e32 v130, v130
	v_exp_f32_e32 v131, v131
	v_exp_f32_e32 v132, v132
	v_exp_f32_e32 v133, v133
	v_exp_f32_e32 v134, v134
	v_exp_f32_e32 v135, v135
	v_exp_f32_e32 v136, v136
	v_exp_f32_e32 v137, v137
	v_exp_f32_e32 v138, v138
	v_exp_f32_e32 v139, v139
	v_exp_f32_e32 v140, v140
	v_exp_f32_e32 v141, v141
	v_exp_f32_e32 v142, v142
	v_exp_f32_e32 v143, v143
	s_cmp_lg_u32 s36, 0
	s_cbranch_scc1 .Lat_m5
	v_mov_b32_e32 v108, 0
	v_mov_b32_e32 v109, 0
	v_mov_b32_e32 v110, 0
	v_mov_b32_e32 v111, 0
	v_mov_b32_e32 v112, 0
	v_mov_b32_e32 v113, 0
	v_mov_b32_e32 v114, 0
	v_mov_b32_e32 v115, 0
	v_mov_b32_e32 v116, 0
	v_mov_b32_e32 v117, 0
	v_mov_b32_e32 v118, 0
	v_mov_b32_e32 v119, 0
.Lat_m5:
	s_nop 0
	v_pk_add_f32 v[232:233], v[108:109], v[110:111]
	v_pk_add_f32 v[234:235], v[112:113], v[114:115]
	v_pk_add_f32 v[232:233], v[232:233], v[116:117]
	v_pk_add_f32 v[234:235], v[234:235], v[118:119]
	v_pk_add_f32 v[232:233], v[232:233], v[120:121]
	v_pk_add_f32 v[234:235], v[234:235], v[122:123]
	v_pk_add_f32 v[232:233], v[232:233], v[124:125]
	v_pk_add_f32 v[234:235], v[234:235], v[126:127]
	v_pk_add_f32 v[232:233], v[232:233], v[128:129]
	v_pk_add_f32 v[234:235], v[234:235], v[130:131]
	v_pk_add_f32 v[232:233], v[232:233], v[132:133]
	v_pk_add_f32 v[234:235], v[234:235], v[134:135]
	v_pk_add_f32 v[232:233], v[232:233], v[136:137]
	v_pk_add_f32 v[234:235], v[234:235], v[138:139]
	v_pk_add_f32 v[232:233], v[232:233], v[140:141]
	v_pk_add_f32 v[234:235], v[234:235], v[142:143]
	v_pk_add_f32 v[232:233], v[232:233], v[234:235]
	s_nop 0
	v_add_f32_e32 v232, v232, v233
	v_cvt_pk_bf16_f32 v108, v108, v109
	v_cvt_pk_bf16_f32 v109, v110, v111
	v_cvt_pk_bf16_f32 v110, v112, v113
	v_cvt_pk_bf16_f32 v111, v114, v115
	v_cvt_pk_bf16_f32 v116, v116, v117
	v_cvt_pk_bf16_f32 v117, v118, v119
	v_cvt_pk_bf16_f32 v118, v120, v121
	v_cvt_pk_bf16_f32 v119, v122, v123
	v_cvt_pk_bf16_f32 v124, v124, v125
	v_cvt_pk_bf16_f32 v125, v126, v127
	v_cvt_pk_bf16_f32 v126, v128, v129
	v_cvt_pk_bf16_f32 v127, v130, v131
	v_cvt_pk_bf16_f32 v132, v132, v133
	v_cvt_pk_bf16_f32 v133, v134, v135
	v_cvt_pk_bf16_f32 v134, v136, v137
	v_cvt_pk_bf16_f32 v135, v138, v139
	v_cvt_pk_bf16_f32 v140, v140, v141
	v_cvt_pk_bf16_f32 v141, v142, v143
	v_mov_b32_e32 v142, 0
	v_mov_b32_e32 v143, 0
	ds_bpermute_b32 v233, v15, v232
	s_waitcnt lgkmcnt(1)
	v_mfma_f32_16x16x32_bf16 v[144:147], v[160:163], v[108:111], 0
	v_mfma_f32_16x16x32_bf16 v[148:151], v[164:167], v[108:111], 0
	v_mfma_f32_16x16x32_bf16 v[152:155], v[168:171], v[108:111], 0
	v_mfma_f32_16x16x32_bf16 v[156:159], v[172:175], v[108:111], 0
	v_mfma_f32_16x16x32_bf16 v[144:147], v[176:179], v[116:119], v[144:147]
	v_mfma_f32_16x16x32_bf16 v[148:151], v[180:183], v[116:119], v[148:151]
	v_mfma_f32_16x16x32_bf16 v[152:155], v[184:187], v[116:119], v[152:155]
	v_mfma_f32_16x16x32_bf16 v[156:159], v[188:191], v[116:119], v[156:159]
	v_mfma_f32_16x16x32_bf16 v[144:147], v[192:195], v[124:127], v[144:147]
	v_mfma_f32_16x16x32_bf16 v[148:151], v[196:199], v[124:127], v[148:151]
	v_mfma_f32_16x16x32_bf16 v[152:155], v[200:203], v[124:127], v[152:155]
	v_mfma_f32_16x16x32_bf16 v[156:159], v[204:207], v[124:127], v[156:159]
	ds_read2_b64 v[160:163], v11 offset0:44 offset1:48
	ds_read2_b64 v[164:167], v12 offset0:44 offset1:48
	ds_read2_b64 v[168:171], v13 offset0:44 offset1:48
	ds_read2_b64 v[172:175], v14 offset0:44 offset1:48
	ds_read2_b64 v[176:179], v11 offset0:52 offset1:52
	ds_read2_b64 v[180:183], v12 offset0:52 offset1:52
	ds_read2_b64 v[184:187], v13 offset0:52 offset1:52
	ds_read2_b64 v[188:191], v14 offset0:52 offset1:52
	s_waitcnt lgkmcnt(8)
	v_add_f32_e32 v232, v232, v233
	s_nop 0
	ds_bpermute_b32 v233, v16, v232
	s_waitcnt lgkmcnt(1)
	v_mfma_f32_16x16x32_bf16 v[144:147], v[160:163], v[132:135], v[144:147]
	v_mfma_f32_16x16x32_bf16 v[148:151], v[164:167], v[132:135], v[148:151]
	v_mfma_f32_16x16x32_bf16 v[152:155], v[168:171], v[132:135], v[152:155]
	v_mfma_f32_16x16x32_bf16 v[156:159], v[172:175], v[132:135], v[156:159]
	v_mfma_f32_16x16x32_bf16 v[144:147], v[176:179], v[140:143], v[144:147]
	v_mfma_f32_16x16x32_bf16 v[148:151], v[180:183], v[140:143], v[148:151]
	v_mfma_f32_16x16x32_bf16 v[152:155], v[184:187], v[140:143], v[152:155]
	v_mfma_f32_16x16x32_bf16 v[156:159], v[188:191], v[140:143], v[156:159]
	s_waitcnt lgkmcnt(0)
	v_add_f32_e32 v232, v232, v233
	v_add_f32_e32 v232, v232, v88
	v_rcp_f32_e32 v236, v232
	s_nop 0
	v_mov_b32_e32 v237, v236
	s_nop 4
	v_pk_mul_f32 v[144:145], v[144:145], v[236:237]
	v_pk_mul_f32 v[146:147], v[146:147], v[236:237]
	v_pk_mul_f32 v[148:149], v[148:149], v[236:237]
	v_pk_mul_f32 v[150:151], v[150:151], v[236:237]
	v_pk_mul_f32 v[152:153], v[152:153], v[236:237]
	v_pk_mul_f32 v[154:155], v[154:155], v[236:237]
	v_pk_mul_f32 v[156:157], v[156:157], v[236:237]
	v_pk_mul_f32 v[158:159], v[158:159], v[236:237]
	v_cvt_pk_bf16_f32 v144, v144, v145
	v_cvt_pk_bf16_f32 v145, v146, v147
	v_cvt_pk_bf16_f32 v148, v148, v149
	v_cvt_pk_bf16_f32 v149, v150, v151
	v_cvt_pk_bf16_f32 v152, v152, v153
	v_cvt_pk_bf16_f32 v153, v154, v155
	v_cvt_pk_bf16_f32 v156, v156, v157
	v_cvt_pk_bf16_f32 v157, v158, v159
	global_store_dwordx2 v9, v[144:145], s[50:51] offset:0
	global_store_dwordx2 v9, v[148:149], s[50:51] offset:32
	global_store_dwordx2 v9, v[152:153], s[50:51] offset:64
	global_store_dwordx2 v9, v[156:157], s[50:51] offset:96
	s_add_u32 s50, s50, 0x10000
	s_addc_u32 s51, s51, 0
	s_add_u32 s48, s48, 0x14000
	s_addc_u32 s49, s49, 0
	ds_read_b128 v[160:163], v10 offset:13824
	ds_read_b128 v[164:167], v10 offset:13888
	ds_read_b128 v[168:171], v10 offset:16128
	ds_read_b128 v[172:175], v10 offset:16192
	ds_read_b128 v[176:179], v10 offset:18432
	ds_read_b128 v[180:183], v10 offset:18496
	ds_read_b128 v[184:187], v10 offset:20736
	ds_read_b128 v[188:191], v10 offset:20800
	ds_read_b128 v[192:195], v10 offset:23040
	ds_read_b128 v[196:199], v10 offset:23104
	s_waitcnt vmcnt(4)
	global_load_dwordx4 v[100:103], v8, s[48:49]
	global_load_dwordx4 v[104:107], v8, s[48:49] offset:64
	v_lshlrev_b32_e32 v234, 16, v92
	v_and_b32_e32 v235, 0xffff0000, v92
	v_pk_mul_f32 v[232:233], v[234:235], v[234:235]
	v_lshlrev_b32_e32 v234, 16, v93
	v_and_b32_e32 v235, 0xffff0000, v93
	v_pk_fma_f32 v[232:233], v[234:235], v[234:235], v[232:233]
	v_lshlrev_b32_e32 v234, 16, v94
	v_and_b32_e32 v235, 0xffff0000, v94
	v_pk_fma_f32 v[232:233], v[234:235], v[234:235], v[232:233]
	v_lshlrev_b32_e32 v234, 16, v95
	v_and_b32_e32 v235, 0xffff0000, v95
	v_pk_fma_f32 v[232:233], v[234:235], v[234:235], v[232:233]
	v_lshlrev_b32_e32 v234, 16, v96
	v_and_b32_e32 v235, 0xffff0000, v96
	v_pk_fma_f32 v[232:233], v[234:235], v[234:235], v[232:233]
	v_lshlrev_b32_e32 v234, 16, v97
	v_and_b32_e32 v235, 0xffff0000, v97
	v_pk_fma_f32 v[232:233], v[234:235], v[234:235], v[232:233]
	v_lshlrev_b32_e32 v234, 16, v98
	v_and_b32_e32 v235, 0xffff0000, v98
	v_pk_fma_f32 v[232:233], v[234:235], v[234:235], v[232:233]
	v_lshlrev_b32_e32 v234, 16, v99
	v_and_b32_e32 v235, 0xffff0000, v99
	v_pk_fma_f32 v[232:233], v[234:235], v[234:235], v[232:233]
	ds_read_b128 v[200:203], v10 offset:25344
	ds_read_b128 v[204:207], v10 offset:25408
	ds_read_b128 v[208:211], v10 offset:27648
	ds_read_b128 v[212:215], v10 offset:27712
	ds_read_b128 v[216:219], v10 offset:29952
	ds_read_b128 v[220:223], v10 offset:30016
	ds_read_b128 v[224:227], v10 offset:32256
	ds_read_b128 v[228:231], v10 offset:32320
	v_add_f32_e32 v232, v232, v233
	s_nop 0
	ds_bpermute_b32 v233, v15, v232
	s_waitcnt lgkmcnt(9)
	v_mfma_f32_16x16x32_bf16 v[108:111], v[160:163], v[92:95], 0
	v_mfma_f32_16x16x32_bf16 v[112:115], v[168:171], v[92:95], 0
	v_mfma_f32_16x16x32_bf16 v[116:119], v[176:179], v[92:95], 0
	v_mfma_f32_16x16x32_bf16 v[120:123], v[184:187], v[92:95], 0
	v_mfma_f32_16x16x32_bf16 v[124:127], v[192:195], v[92:95], 0
	v_mfma_f32_16x16x32_bf16 v[108:111], v[164:167], v[96:99], v[108:111]
	v_mfma_f32_16x16x32_bf16 v[112:115], v[172:175], v[96:99], v[112:115]
	v_mfma_f32_16x16x32_bf16 v[116:119], v[180:183], v[96:99], v[116:119]
	v_mfma_f32_16x16x32_bf16 v[120:123], v[188:191], v[96:99], v[120:123]
	v_mfma_f32_16x16x32_bf16 v[124:127], v[196:199], v[96:99], v[124:127]
	s_waitcnt lgkmcnt(0)
	v_add_f32_e32 v232, v232, v233
	v_mfma_f32_16x16x32_bf16 v[128:131], v[200:203], v[92:95], 0
	v_mfma_f32_16x16x32_bf16 v[132:135], v[208:211], v[92:95], 0
	v_mfma_f32_16x16x32_bf16 v[136:139], v[216:219], v[92:95], 0
	v_mfma_f32_16x16x32_bf16 v[140:143], v[224:227], v[92:95], 0
	ds_bpermute_b32 v233, v16, v232
	v_mfma_f32_16x16x32_bf16 v[128:131], v[204:207], v[96:99], v[128:131]
	v_mfma_f32_16x16x32_bf16 v[132:135], v[212:215], v[96:99], v[132:135]
	v_mfma_f32_16x16x32_bf16 v[136:139], v[220:223], v[96:99], v[136:139]
	v_mfma_f32_16x16x32_bf16 v[140:143], v[228:231], v[96:99], v[140:143]
	ds_read2_b64 v[160:163], v11 offset0:24 offset1:28
	ds_read2_b64 v[164:167], v12 offset0:24 offset1:28
	ds_read2_b64 v[168:171], v13 offset0:24 offset1:28
	ds_read2_b64 v[172:175], v14 offset0:24 offset1:28
	ds_read2_b64 v[176:179], v11 offset0:32 offset1:36
	ds_read2_b64 v[180:183], v12 offset0:32 offset1:36
	ds_read2_b64 v[184:187], v13 offset0:32 offset1:36
	ds_read2_b64 v[188:191], v14 offset0:32 offset1:36
	ds_read2_b64 v[192:195], v11 offset0:40 offset1:44
	ds_read2_b64 v[196:199], v12 offset0:40 offset1:44
	ds_read2_b64 v[200:203], v13 offset0:40 offset1:44
	ds_read2_b64 v[204:207], v14 offset0:40 offset1:44
	s_waitcnt lgkmcnt(12)
	v_add_f32_e32 v232, v232, v233
	v_mul_f32_e32 v232, 0x3c800000, v232
	v_add_f32_e32 v232, 0x358637bd, v232
	v_rsq_f32_e32 v236, v232
	s_nop 0
	v_mov_b32_e32 v237, v236
	s_nop 1
	v_pk_fma_f32 v[108:109], v[108:109], v[236:237], v[52:53]
	v_pk_fma_f32 v[110:111], v[110:111], v[236:237], v[54:55]
	v_pk_fma_f32 v[112:113], v[112:113], v[236:237], v[56:57]
	v_pk_fma_f32 v[114:115], v[114:115], v[236:237], v[58:59]
	v_pk_fma_f32 v[116:117], v[116:117], v[236:237], v[60:61]
	v_pk_fma_f32 v[118:119], v[118:119], v[236:237], v[62:63]
	v_pk_fma_f32 v[120:121], v[120:121], v[236:237], v[64:65]
	v_pk_fma_f32 v[122:123], v[122:123], v[236:237], v[66:67]
	v_pk_fma_f32 v[124:125], v[124:125], v[236:237], v[68:69]
	v_pk_fma_f32 v[126:127], v[126:127], v[236:237], v[70:71]
	v_pk_fma_f32 v[128:129], v[128:129], v[236:237], v[72:73]
	v_pk_fma_f32 v[130:131], v[130:131], v[236:237], v[74:75]
	v_pk_fma_f32 v[132:133], v[132:133], v[236:237], v[76:77]
	v_pk_fma_f32 v[134:135], v[134:135], v[236:237], v[78:79]
	v_pk_fma_f32 v[136:137], v[136:137], v[236:237], v[80:81]
	v_pk_fma_f32 v[138:139], v[138:139], v[236:237], v[82:83]
	v_pk_fma_f32 v[140:141], v[140:141], v[236:237], v[84:85]
	v_pk_fma_f32 v[142:143], v[142:143], v[236:237], v[86:87]
	v_exp_f32_e32 v108, v108
	v_exp_f32_e32 v109, v109
	v_exp_f32_e32 v110, v110
	v_exp_f32_e32 v111, v111
	v_exp_f32_e32 v112, v112
	v_exp_f32_e32 v113, v113
	v_exp_f32_e32 v114, v114
	v_exp_f32_e32 v115, v115
	v_exp_f32_e32 v116, v116
	v_exp_f32_e32 v117, v117
	v_exp_f32_e32 v118, v118
	v_exp_f32_e32 v119, v119
	v_exp_f32_e32 v120, v120
	v_exp_f32_e32 v121, v121
	v_exp_f32_e32 v122, v122
	v_exp_f32_e32 v123, v123
	v_exp_f32_e32 v124, v124
	v_exp_f32_e32 v125, v125
	v_exp_f32_e32 v126, v126
	v_exp_f32_e32 v127, v127
	v_exp_f32_e32 v128, v128
	v_exp_f32_e32 v129, v129
	v_exp_f32_e32 v130, v130
	v_exp_f32_e32 v131, v131
	v_exp_f32_e32 v132, v132
	v_exp_f32_e32 v133, v133
	v_exp_f32_e32 v134, v134
	v_exp_f32_e32 v135, v135
	v_exp_f32_e32 v136, v136
	v_exp_f32_e32 v137, v137
	v_exp_f32_e32 v138, v138
	v_exp_f32_e32 v139, v139
	v_exp_f32_e32 v140, v140
	v_exp_f32_e32 v141, v141
	v_exp_f32_e32 v142, v142
	v_exp_f32_e32 v143, v143
	s_cmp_lg_u32 s36, 0
	s_cbranch_scc1 .Lat_m6
	v_mov_b32_e32 v108, 0
	v_mov_b32_e32 v109, 0
	v_mov_b32_e32 v110, 0
	v_mov_b32_e32 v111, 0
	v_mov_b32_e32 v112, 0
	v_mov_b32_e32 v113, 0
	v_mov_b32_e32 v114, 0
	v_mov_b32_e32 v115, 0
.Lat_m6:
	s_nop 0
	v_pk_add_f32 v[232:233], v[108:109], v[110:111]
	v_pk_add_f32 v[234:235], v[112:113], v[114:115]
	v_pk_add_f32 v[232:233], v[232:233], v[116:117]
	v_pk_add_f32 v[234:235], v[234:235], v[118:119]
	v_pk_add_f32 v[232:233], v[232:233], v[120:121]
	v_pk_add_f32 v[234:235], v[234:235], v[122:123]
	v_pk_add_f32 v[232:233], v[232:233], v[124:125]
	v_pk_add_f32 v[234:235], v[234:235], v[126:127]
	v_pk_add_f32 v[232:233], v[232:233], v[128:129]
	v_pk_add_f32 v[234:235], v[234:235], v[130:131]
	v_pk_add_f32 v[232:233], v[232:233], v[132:133]
	v_pk_add_f32 v[234:235], v[234:235], v[134:135]
	v_pk_add_f32 v[232:233], v[232:233], v[136:137]
	v_pk_add_f32 v[234:235], v[234:235], v[138:139]
	v_pk_add_f32 v[232:233], v[232:233], v[140:141]
	v_pk_add_f32 v[234:235], v[234:235], v[142:143]
	v_pk_add_f32 v[232:233], v[232:233], v[234:235]
	s_nop 0
	v_add_f32_e32 v232, v232, v233
	v_cvt_pk_bf16_f32 v108, v108, v109
	v_cvt_pk_bf16_f32 v109, v110, v111
	v_cvt_pk_bf16_f32 v110, v112, v113
	v_cvt_pk_bf16_f32 v111, v114, v115
	v_cvt_pk_bf16_f32 v116, v116, v117
	v_cvt_pk_bf16_f32 v117, v118, v119
	v_cvt_pk_bf16_f32 v118, v120, v121
	v_cvt_pk_bf16_f32 v119, v122, v123
	v_cvt_pk_bf16_f32 v124, v124, v125
	v_cvt_pk_bf16_f32 v125, v126, v127
	v_cvt_pk_bf16_f32 v126, v128, v129
	v_cvt_pk_bf16_f32 v127, v130, v131
	v_cvt_pk_bf16_f32 v132, v132, v133
	v_cvt_pk_bf16_f32 v133, v134, v135
	v_cvt_pk_bf16_f32 v134, v136, v137
	v_cvt_pk_bf16_f32 v135, v138, v139
	v_cvt_pk_bf16_f32 v140, v140, v141
	v_cvt_pk_bf16_f32 v141, v142, v143
	v_mov_b32_e32 v142, 0
	v_mov_b32_e32 v143, 0
	ds_bpermute_b32 v233, v15, v232
	s_waitcnt lgkmcnt(1)
	v_mfma_f32_16x16x32_bf16 v[144:147], v[160:163], v[108:111], 0
	v_mfma_f32_16x16x32_bf16 v[148:151], v[164:167], v[108:111], 0
	v_mfma_f32_16x16x32_bf16 v[152:155], v[168:171], v[108:111], 0
	v_mfma_f32_16x16x32_bf16 v[156:159], v[172:175], v[108:111], 0
	v_mfma_f32_16x16x32_bf16 v[144:147], v[176:179], v[116:119], v[144:147]
	v_mfma_f32_16x16x32_bf16 v[148:151], v[180:183], v[116:119], v[148:151]
	v_mfma_f32_16x16x32_bf16 v[152:155], v[184:187], v[116:119], v[152:155]
	v_mfma_f32_16x16x32_bf16 v[156:159], v[188:191], v[116:119], v[156:159]
	v_mfma_f32_16x16x32_bf16 v[144:147], v[192:195], v[124:127], v[144:147]
	v_mfma_f32_16x16x32_bf16 v[148:151], v[196:199], v[124:127], v[148:151]
	v_mfma_f32_16x16x32_bf16 v[152:155], v[200:203], v[124:127], v[152:155]
	v_mfma_f32_16x16x32_bf16 v[156:159], v[204:207], v[124:127], v[156:159]
	ds_read2_b64 v[160:163], v11 offset0:48 offset1:52
	ds_read2_b64 v[164:167], v12 offset0:48 offset1:52
	ds_read2_b64 v[168:171], v13 offset0:48 offset1:52
	ds_read2_b64 v[172:175], v14 offset0:48 offset1:52
	ds_read2_b64 v[176:179], v11 offset0:56 offset1:56
	ds_read2_b64 v[180:183], v12 offset0:56 offset1:56
	ds_read2_b64 v[184:187], v13 offset0:56 offset1:56
	ds_read2_b64 v[188:191], v14 offset0:56 offset1:56
	s_waitcnt lgkmcnt(8)
	v_add_f32_e32 v232, v232, v233
	s_nop 0
	ds_bpermute_b32 v233, v16, v232
	s_waitcnt lgkmcnt(1)
	v_mfma_f32_16x16x32_bf16 v[144:147], v[160:163], v[132:135], v[144:147]
	v_mfma_f32_16x16x32_bf16 v[148:151], v[164:167], v[132:135], v[148:151]
	v_mfma_f32_16x16x32_bf16 v[152:155], v[168:171], v[132:135], v[152:155]
	v_mfma_f32_16x16x32_bf16 v[156:159], v[172:175], v[132:135], v[156:159]
	v_mfma_f32_16x16x32_bf16 v[144:147], v[176:179], v[140:143], v[144:147]
	v_mfma_f32_16x16x32_bf16 v[148:151], v[180:183], v[140:143], v[148:151]
	v_mfma_f32_16x16x32_bf16 v[152:155], v[184:187], v[140:143], v[152:155]
	v_mfma_f32_16x16x32_bf16 v[156:159], v[188:191], v[140:143], v[156:159]
	s_waitcnt lgkmcnt(0)
	v_add_f32_e32 v232, v232, v233
	v_add_f32_e32 v232, v232, v88
	v_rcp_f32_e32 v236, v232
	s_nop 0
	v_mov_b32_e32 v237, v236
	s_nop 4
	v_pk_mul_f32 v[144:145], v[144:145], v[236:237]
	v_pk_mul_f32 v[146:147], v[146:147], v[236:237]
	v_pk_mul_f32 v[148:149], v[148:149], v[236:237]
	v_pk_mul_f32 v[150:151], v[150:151], v[236:237]
	v_pk_mul_f32 v[152:153], v[152:153], v[236:237]
	v_pk_mul_f32 v[154:155], v[154:155], v[236:237]
	v_pk_mul_f32 v[156:157], v[156:157], v[236:237]
	v_pk_mul_f32 v[158:159], v[158:159], v[236:237]
	v_cvt_pk_bf16_f32 v144, v144, v145
	v_cvt_pk_bf16_f32 v145, v146, v147
	v_cvt_pk_bf16_f32 v148, v148, v149
	v_cvt_pk_bf16_f32 v149, v150, v151
	v_cvt_pk_bf16_f32 v152, v152, v153
	v_cvt_pk_bf16_f32 v153, v154, v155
	v_cvt_pk_bf16_f32 v156, v156, v157
	v_cvt_pk_bf16_f32 v157, v158, v159
	global_store_dwordx2 v9, v[144:145], s[50:51] offset:0
	global_store_dwordx2 v9, v[148:149], s[50:51] offset:32
	global_store_dwordx2 v9, v[152:153], s[50:51] offset:64
	global_store_dwordx2 v9, v[156:157], s[50:51] offset:96
	s_add_u32 s50, s50, 0x10000
	s_addc_u32 s51, s51, 0
	ds_read_b128 v[160:163], v10 offset:16128
	ds_read_b128 v[164:167], v10 offset:16192
	ds_read_b128 v[168:171], v10 offset:18432
	ds_read_b128 v[172:175], v10 offset:18496
	ds_read_b128 v[176:179], v10 offset:20736
	ds_read_b128 v[180:183], v10 offset:20800
	ds_read_b128 v[184:187], v10 offset:23040
	ds_read_b128 v[188:191], v10 offset:23104
	ds_read_b128 v[192:195], v10 offset:25344
	ds_read_b128 v[196:199], v10 offset:25408
	s_waitcnt vmcnt(4)
	v_lshlrev_b32_e32 v234, 16, v100
	v_and_b32_e32 v235, 0xffff0000, v100
	v_pk_mul_f32 v[232:233], v[234:235], v[234:235]
	v_lshlrev_b32_e32 v234, 16, v101
	v_and_b32_e32 v235, 0xffff0000, v101
	v_pk_fma_f32 v[232:233], v[234:235], v[234:235], v[232:233]
	v_lshlrev_b32_e32 v234, 16, v102
	v_and_b32_e32 v235, 0xffff0000, v102
	v_pk_fma_f32 v[232:233], v[234:235], v[234:235], v[232:233]
	v_lshlrev_b32_e32 v234, 16, v103
	v_and_b32_e32 v235, 0xffff0000, v103
	v_pk_fma_f32 v[232:233], v[234:235], v[234:235], v[232:233]
	v_lshlrev_b32_e32 v234, 16, v104
	v_and_b32_e32 v235, 0xffff0000, v104
	v_pk_fma_f32 v[232:233], v[234:235], v[234:235], v[232:233]
	v_lshlrev_b32_e32 v234, 16, v105
	v_and_b32_e32 v235, 0xffff0000, v105
	v_pk_fma_f32 v[232:233], v[234:235], v[234:235], v[232:233]
	v_lshlrev_b32_e32 v234, 16, v106
	v_and_b32_e32 v235, 0xffff0000, v106
	v_pk_fma_f32 v[232:233], v[234:235], v[234:235], v[232:233]
	v_lshlrev_b32_e32 v234, 16, v107
	v_and_b32_e32 v235, 0xffff0000, v107
	v_pk_fma_f32 v[232:233], v[234:235], v[234:235], v[232:233]
	ds_read_b128 v[200:203], v10 offset:27648
	ds_read_b128 v[204:207], v10 offset:27712
	ds_read_b128 v[208:211], v10 offset:29952
	ds_read_b128 v[212:215], v10 offset:30016
	ds_read_b128 v[216:219], v10 offset:32256
	ds_read_b128 v[220:223], v10 offset:32320
	ds_read_b128 v[224:227], v10 offset:34560
	ds_read_b128 v[228:231], v10 offset:34624
	v_add_f32_e32 v232, v232, v233
	s_nop 0
	ds_bpermute_b32 v233, v15, v232
	s_waitcnt lgkmcnt(9)
	v_mfma_f32_16x16x32_bf16 v[108:111], v[160:163], v[100:103], 0
	v_mfma_f32_16x16x32_bf16 v[112:115], v[168:171], v[100:103], 0
	v_mfma_f32_16x16x32_bf16 v[116:119], v[176:179], v[100:103], 0
	v_mfma_f32_16x16x32_bf16 v[120:123], v[184:187], v[100:103], 0
	v_mfma_f32_16x16x32_bf16 v[124:127], v[192:195], v[100:103], 0
	v_mfma_f32_16x16x32_bf16 v[108:111], v[164:167], v[104:107], v[108:111]
	v_mfma_f32_16x16x32_bf16 v[112:115], v[172:175], v[104:107], v[112:115]
	v_mfma_f32_16x16x32_bf16 v[116:119], v[180:183], v[104:107], v[116:119]
	v_mfma_f32_16x16x32_bf16 v[120:123], v[188:191], v[104:107], v[120:123]
	v_mfma_f32_16x16x32_bf16 v[124:127], v[196:199], v[104:107], v[124:127]
	s_waitcnt lgkmcnt(0)
	v_add_f32_e32 v232, v232, v233
	v_mfma_f32_16x16x32_bf16 v[128:131], v[200:203], v[100:103], 0
	v_mfma_f32_16x16x32_bf16 v[132:135], v[208:211], v[100:103], 0
	v_mfma_f32_16x16x32_bf16 v[136:139], v[216:219], v[100:103], 0
	v_mfma_f32_16x16x32_bf16 v[140:143], v[224:227], v[100:103], 0
	ds_bpermute_b32 v233, v16, v232
	v_mfma_f32_16x16x32_bf16 v[128:131], v[204:207], v[104:107], v[128:131]
	v_mfma_f32_16x16x32_bf16 v[132:135], v[212:215], v[104:107], v[132:135]
	v_mfma_f32_16x16x32_bf16 v[136:139], v[220:223], v[104:107], v[136:139]
	v_mfma_f32_16x16x32_bf16 v[140:143], v[228:231], v[104:107], v[140:143]
	ds_read2_b64 v[160:163], v11 offset0:28 offset1:32
	ds_read2_b64 v[164:167], v12 offset0:28 offset1:32
	ds_read2_b64 v[168:171], v13 offset0:28 offset1:32
	ds_read2_b64 v[172:175], v14 offset0:28 offset1:32
	ds_read2_b64 v[176:179], v11 offset0:36 offset1:40
	ds_read2_b64 v[180:183], v12 offset0:36 offset1:40
	ds_read2_b64 v[184:187], v13 offset0:36 offset1:40
	ds_read2_b64 v[188:191], v14 offset0:36 offset1:40
	ds_read2_b64 v[192:195], v11 offset0:44 offset1:48
	ds_read2_b64 v[196:199], v12 offset0:44 offset1:48
	ds_read2_b64 v[200:203], v13 offset0:44 offset1:48
	ds_read2_b64 v[204:207], v14 offset0:44 offset1:48
	s_waitcnt lgkmcnt(12)
	v_add_f32_e32 v232, v232, v233
	v_mul_f32_e32 v232, 0x3c800000, v232
	v_add_f32_e32 v232, 0x358637bd, v232
	v_rsq_f32_e32 v236, v232
	s_nop 0
	v_mov_b32_e32 v237, v236
	s_nop 1
	v_pk_fma_f32 v[108:109], v[108:109], v[236:237], v[52:53]
	v_pk_fma_f32 v[110:111], v[110:111], v[236:237], v[54:55]
	v_pk_fma_f32 v[112:113], v[112:113], v[236:237], v[56:57]
	v_pk_fma_f32 v[114:115], v[114:115], v[236:237], v[58:59]
	v_pk_fma_f32 v[116:117], v[116:117], v[236:237], v[60:61]
	v_pk_fma_f32 v[118:119], v[118:119], v[236:237], v[62:63]
	v_pk_fma_f32 v[120:121], v[120:121], v[236:237], v[64:65]
	v_pk_fma_f32 v[122:123], v[122:123], v[236:237], v[66:67]
	v_pk_fma_f32 v[124:125], v[124:125], v[236:237], v[68:69]
	v_pk_fma_f32 v[126:127], v[126:127], v[236:237], v[70:71]
	v_pk_fma_f32 v[128:129], v[128:129], v[236:237], v[72:73]
	v_pk_fma_f32 v[130:131], v[130:131], v[236:237], v[74:75]
	v_pk_fma_f32 v[132:133], v[132:133], v[236:237], v[76:77]
	v_pk_fma_f32 v[134:135], v[134:135], v[236:237], v[78:79]
	v_pk_fma_f32 v[136:137], v[136:137], v[236:237], v[80:81]
	v_pk_fma_f32 v[138:139], v[138:139], v[236:237], v[82:83]
	v_pk_fma_f32 v[140:141], v[140:141], v[236:237], v[84:85]
	v_pk_fma_f32 v[142:143], v[142:143], v[236:237], v[86:87]
	v_exp_f32_e32 v108, v108
	v_exp_f32_e32 v109, v109
	v_exp_f32_e32 v110, v110
	v_exp_f32_e32 v111, v111
	v_exp_f32_e32 v112, v112
	v_exp_f32_e32 v113, v113
	v_exp_f32_e32 v114, v114
	v_exp_f32_e32 v115, v115
	v_exp_f32_e32 v116, v116
	v_exp_f32_e32 v117, v117
	v_exp_f32_e32 v118, v118
	v_exp_f32_e32 v119, v119
	v_exp_f32_e32 v120, v120
	v_exp_f32_e32 v121, v121
	v_exp_f32_e32 v122, v122
	v_exp_f32_e32 v123, v123
	v_exp_f32_e32 v124, v124
	v_exp_f32_e32 v125, v125
	v_exp_f32_e32 v126, v126
	v_exp_f32_e32 v127, v127
	v_exp_f32_e32 v128, v128
	v_exp_f32_e32 v129, v129
	v_exp_f32_e32 v130, v130
	v_exp_f32_e32 v131, v131
	v_exp_f32_e32 v132, v132
	v_exp_f32_e32 v133, v133
	v_exp_f32_e32 v134, v134
	v_exp_f32_e32 v135, v135
	v_exp_f32_e32 v136, v136
	v_exp_f32_e32 v137, v137
	v_exp_f32_e32 v138, v138
	v_exp_f32_e32 v139, v139
	v_exp_f32_e32 v140, v140
	v_exp_f32_e32 v141, v141
	v_exp_f32_e32 v142, v142
	v_exp_f32_e32 v143, v143
	s_cmp_lg_u32 s36, 0
	s_cbranch_scc1 .Lat_m7
	v_mov_b32_e32 v108, 0
	v_mov_b32_e32 v109, 0
	v_mov_b32_e32 v110, 0
	v_mov_b32_e32 v111, 0
